# mLSTM output loop: sigmoid division and scaling chains as packed-f32 ops, same per-element operations
# baseline (speedup 1.0000x reference)
; #define LAS __attribute__((address_space(3)))
; __device__ __forceinline__ bf16_t f2bf(float f) { unsigned u = __builtin_bit_cast(unsigned, f); return (bf16_t)((u + 0x7fffu + ((u >> 16) & 1u)) >> 16); }
; __device__ __forceinline__ int crow(int r, int hi) { return (r & 3) + 8 * (r >> 2) + 4 * hi; }
; __device__ __forceinline__ int crow(int r, int hi) { return (r & 3) + 8 * (r >> 2) + 4 * hi; }
; __device__ __forceinline__ void out_unit_m(LAS unsigned char* lds, LAS unsigned char* ldstab, const OutArgs a, const int wv) {
;     ...
;     __syncthreads();
;     constexpr int TP = DV * 2;
; #pragma unroll
;     for (int r = 0; r < 16; ++r) { const int row = 32 * rb + crow(r, hi);
;         const float inv = rsqrtf((s2[r] + exch[(1 - dh) * 128 + row]) * (1.f / DV) + EPS);
; #pragma unroll
;         for (int nb = 0; nb < 2; ++nb) *(LAS bf16_t*)(lds + row * TP + (dh * 64 + 32 * nb + r32) * 2) = f2bf(o[nb][r] * inv); }
.LBB0_648:
	s_or_b64 exec, exec, s[6:7]
	v_or_b32_e32 v56, s12, v156
	s_lshl_b32 s6, s8, 7
	v_subrev_u32_e32 v48, s6, v56
	s_add_i32 s7, 0, 0x22100
	v_lshl_add_u32 v48, v48, 2, s7
	s_waitcnt lgkmcnt(0)
	s_barrier
	ds_read_b128 v[48:51], v48 offset:512
	v_or_b32_e32 v57, 8, v56
	v_subrev_u32_e32 v52, s6, v57
	v_lshl_add_u32 v52, v52, 2, s7
	ds_read_b128 v[52:55], v52 offset:512
	s_waitcnt lgkmcnt(1)
	v_pk_add_f32 v[48:49], v[44:45], v[48:49]
	v_mov_b64_e32 v[44:45], s[46:47]
	v_pk_fma_f32 v[48:49], v[48:49], s[44:45], v[44:45] op_sel_hi:[1,0,0]
	v_lshlrev_b32_e32 v59, 1, v159
	v_mul_f32_e32 v58, 0x4b800000, v48
	v_cmp_gt_f32_e32 vcc, s83, v48
	s_add_i32 s8, s6, 0
	s_nop 0
	v_cndmask_b32_e32 v48, v48, v58, vcc
	v_rsq_f32_e32 v48, v48
	v_lshlrev_b32_e32 v58, 8, v56
	v_add3_u32 v58, s8, v58, v59
	v_mul_f32_e32 v60, 0x45800000, v48
	v_cndmask_b32_e32 v48, v48, v60, vcc
	v_mul_f32_e32 v0, v0, v48
	v_bfe_u32 v60, v0, 16, 1
	v_add3_u32 v0, v0, v60, s84
	ds_write_b16_d16_hi v58, v0
	v_mul_f32_e32 v0, v16, v48
	v_mul_f32_e32 v16, 0x4b800000, v49
	v_cmp_gt_f32_e32 vcc, s83, v49
	v_bfe_u32 v48, v0, 16, 1
	v_add3_u32 v0, v0, v48, s84
	v_cndmask_b32_e32 v16, v49, v16, vcc
	v_rsq_f32_e32 v16, v16
	ds_write_b16_d16_hi v58, v0 offset:64
	v_mul_f32_e32 v0, 0x45800000, v16
	v_cndmask_b32_e32 v0, v16, v0, vcc
	v_mul_f32_e32 v1, v1, v0
	v_bfe_u32 v16, v1, 16, 1
	v_add3_u32 v1, v1, v16, s84
	ds_write_b16_d16_hi v58, v1 offset:256
	v_mul_f32_e32 v16, v17, v0
	v_pk_add_f32 v[0:1], v[46:47], v[50:51]
	s_nop 0
	v_pk_fma_f32 v[0:1], v[0:1], s[44:45], v[44:45] op_sel_hi:[1,0,0]
	s_nop 0
	v_mul_f32_e32 v17, 0x4b800000, v0
	v_cmp_gt_f32_e32 vcc, s83, v0
	s_nop 1
	v_cndmask_b32_e32 v0, v0, v17, vcc
	v_rsq_f32_e32 v0, v0
	v_bfe_u32 v17, v16, 16, 1
	v_add3_u32 v16, v16, v17, s84
	ds_write_b16_d16_hi v58, v16 offset:320
	v_mul_f32_e32 v16, 0x45800000, v0
	v_cndmask_b32_e32 v0, v0, v16, vcc
	v_mul_f32_e32 v2, v2, v0
	v_bfe_u32 v16, v2, 16, 1
	v_add3_u32 v2, v2, v16, s84
	ds_write_b16_d16_hi v58, v2 offset:512
	v_mul_f32_e32 v2, 0x4b800000, v1
	v_cmp_gt_f32_e32 vcc, s83, v1
	v_mul_f32_e32 v0, v18, v0
	v_or_b32_e32 v17, 16, v56
	v_cndmask_b32_e32 v1, v1, v2, vcc
	v_rsq_f32_e32 v1, v1
	v_bfe_u32 v2, v0, 16, 1
	v_add3_u32 v0, v0, v2, s84
	ds_write_b16_d16_hi v58, v0 offset:576
	v_mul_f32_e32 v0, 0x45800000, v1
	v_cndmask_b32_e32 v0, v1, v0, vcc
	v_mul_f32_e32 v1, v3, v0
	v_bfe_u32 v2, v1, 16, 1
	v_add3_u32 v1, v1, v2, s84
	v_mul_f32_e32 v0, v19, v0
	ds_write_b16_d16_hi v58, v1 offset:768
	v_bfe_u32 v1, v0, 16, 1
	v_add3_u32 v2, v0, v1, s84
	s_waitcnt lgkmcnt(7)
	v_pk_add_f32 v[0:1], v[40:41], v[52:53]
	ds_write_b16_d16_hi v58, v2 offset:832
	v_pk_fma_f32 v[0:1], v[0:1], s[44:45], v[44:45] op_sel_hi:[1,0,0]
	v_lshlrev_b32_e32 v2, 8, v57
	v_mul_f32_e32 v3, 0x4b800000, v0
	v_cmp_gt_f32_e32 vcc, s83, v0
	v_add3_u32 v2, s8, v2, v59
	v_or_b32_e32 v18, 24, v56
	v_cndmask_b32_e32 v0, v0, v3, vcc
	v_rsq_f32_e32 v0, v0
	s_nop 0
	v_mul_f32_e32 v3, 0x45800000, v0
	v_cndmask_b32_e32 v0, v0, v3, vcc
	v_mul_f32_e32 v3, v4, v0
	v_bfe_u32 v4, v3, 16, 1
	v_add3_u32 v3, v3, v4, s84
	ds_write_b16_d16_hi v2, v3
	v_mul_f32_e32 v3, 0x4b800000, v1
	v_cmp_gt_f32_e32 vcc, s83, v1
	v_mul_f32_e32 v0, v20, v0
	v_subrev_u32_e32 v4, s6, v18
	v_cndmask_b32_e32 v1, v1, v3, vcc
	v_rsq_f32_e32 v1, v1
	v_bfe_u32 v3, v0, 16, 1
	v_add3_u32 v0, v0, v3, s84
	ds_write_b16_d16_hi v2, v0 offset:64
	v_mul_f32_e32 v0, 0x45800000, v1
	v_cndmask_b32_e32 v0, v1, v0, vcc
	v_mul_f32_e32 v1, v5, v0
	v_bfe_u32 v2, v1, 16, 1
	v_add3_u32 v1, v1, v2, s84
	ds_write_b16_d16_hi v58, v1 offset:2304
	v_mul_f32_e32 v2, v21, v0
	v_pk_add_f32 v[0:1], v[42:43], v[54:55]
	v_lshl_add_u32 v4, v4, 2, s7
	v_pk_fma_f32 v[0:1], v[0:1], s[44:45], v[44:45] op_sel_hi:[1,0,0]
	s_nop 0
	v_mul_f32_e32 v3, 0x4b800000, v0
	v_cmp_gt_f32_e32 vcc, s83, v0
	s_nop 1
	v_cndmask_b32_e32 v0, v0, v3, vcc
	v_rsq_f32_e32 v0, v0
	v_bfe_u32 v3, v2, 16, 1
	v_add3_u32 v2, v2, v3, s84
	ds_write_b16_d16_hi v58, v2 offset:2368
	v_mul_f32_e32 v2, 0x45800000, v0
	v_cndmask_b32_e32 v0, v0, v2, vcc
	v_mul_f32_e32 v2, v6, v0
	v_bfe_u32 v3, v2, 16, 1
	v_add3_u32 v2, v2, v3, s84
	ds_write_b16_d16_hi v58, v2 offset:2560
	v_mul_f32_e32 v2, 0x4b800000, v1
	v_cmp_gt_f32_e32 vcc, s83, v1
	v_mul_f32_e32 v0, v22, v0
	s_nop 0
	v_cndmask_b32_e32 v1, v1, v2, vcc
	v_rsq_f32_e32 v1, v1
	v_bfe_u32 v2, v0, 16, 1
	v_add3_u32 v0, v0, v2, s84
	ds_write_b16_d16_hi v58, v0 offset:2624
	v_mul_f32_e32 v0, 0x45800000, v1
	v_cndmask_b32_e32 v0, v1, v0, vcc
	v_mul_f32_e32 v1, v7, v0
	v_bfe_u32 v2, v1, 16, 1
	v_add3_u32 v1, v1, v2, s84
	v_mul_f32_e32 v0, v23, v0
	ds_write_b16_d16_hi v58, v1 offset:2816
	v_bfe_u32 v1, v0, 16, 1
	v_add3_u32 v16, v0, v1, s84
	v_subrev_u32_e32 v0, s6, v17
	v_lshl_add_u32 v0, v0, 2, s7
	ds_read_b128 v[0:3], v0 offset:512
	ds_read_b128 v[4:7], v4 offset:512
	ds_write_b16_d16_hi v58, v16 offset:2880
	v_lshlrev_b32_e32 v16, 8, v17
	v_add3_u32 v16, s8, v16, v59
	s_waitcnt lgkmcnt(2)
; #define LAS __attribute__((address_space(3)))
; __device__ __forceinline__ bf16_t f2bf(float f) { unsigned u = __builtin_bit_cast(unsigned, f); return (bf16_t)((u + 0x7fffu + ((u >> 16) & 1u)) >> 16); }
; __device__ __forceinline__ int crow(int r, int hi) { return (r & 3) + 8 * (r >> 2) + 4 * hi; }
; __device__ __forceinline__ int crow(int r, int hi) { return (r & 3) + 8 * (r >> 2) + 4 * hi; }
; __device__ __forceinline__ void out_unit_m(LAS unsigned char* lds, LAS unsigned char* ldstab, const OutArgs a, const int wv) {
;     ...
; #pragma unroll
;     for (int r = 0; r < 16; ++r) { const int row = 32 * rb + crow(r, hi);
;         const float inv = rsqrtf((s2[r] + exch[(1 - dh) * 128 + row]) * (1.f / DV) + EPS);
; #pragma unroll
;         for (int nb = 0; nb < 2; ++nb) *(LAS bf16_t*)(lds + row * TP + (dh * 64 + 32 * nb + r32) * 2) = f2bf(o[nb][r] * inv); }
;     __syncthreads();
; #pragma unroll 1
;     for (int id = tid; id < 128 * 16; id += 512) { const int row = id >> 4, ch = id & 15;
;         const u32x4 y = *(const LAS u32x4*)(lds + row * TP + ch * 16); const u32x4 g = *(const u32x4*)(a.G + (size_t)row * a.ldg + 8 * ch);
;         const f32x4 g0 = *(const f32x4*)(a.gain + 8 * ch), g1 = *(const f32x4*)(a.gain + 8 * ch + 4);
;         const float yv[8] = {bf_lo(y.x), bf_hi(y.x), bf_lo(y.y), bf_hi(y.y), bf_lo(y.z), bf_hi(y.z), bf_lo(y.w), bf_hi(y.w)};
;         const float gv[8] = {bf_lo(g.x), bf_hi(g.x), bf_lo(g.y), bf_hi(g.y), bf_lo(g.z), bf_hi(g.z), bf_lo(g.w), bf_hi(g.w)};
	v_pk_add_f32 v[0:1], v[36:37], v[0:1]
	s_nop 0
	v_pk_fma_f32 v[0:1], v[0:1], s[44:45], v[44:45] op_sel_hi:[1,0,0]
	s_nop 0
	v_mul_f32_e32 v19, 0x4b800000, v0
	v_cmp_gt_f32_e32 vcc, s83, v0
	s_nop 1
	v_cndmask_b32_e32 v0, v0, v19, vcc
	v_rsq_f32_e32 v0, v0
	s_nop 0
	v_mul_f32_e32 v17, 0x45800000, v0
	v_cndmask_b32_e32 v0, v0, v17, vcc
	v_mul_f32_e32 v8, v8, v0
	v_bfe_u32 v17, v8, 16, 1
	v_add3_u32 v8, v8, v17, s84
	ds_write_b16_d16_hi v16, v8
	v_mul_f32_e32 v8, 0x4b800000, v1
	v_cmp_gt_f32_e32 vcc, s83, v1
	v_mul_f32_e32 v0, v24, v0
	s_nop 0
	v_cndmask_b32_e32 v1, v1, v8, vcc
	v_rsq_f32_e32 v1, v1
	v_bfe_u32 v8, v0, 16, 1
	v_add3_u32 v0, v0, v8, s84
	ds_write_b16_d16_hi v16, v0 offset:64
	v_mul_f32_e32 v0, 0x45800000, v1
	v_cndmask_b32_e32 v0, v1, v0, vcc
	v_mul_f32_e32 v1, v9, v0
	v_bfe_u32 v8, v1, 16, 1
	v_add3_u32 v1, v1, v8, s84
	ds_write_b16_d16_hi v58, v1 offset:4352
	v_mul_f32_e32 v8, v25, v0
	v_pk_add_f32 v[0:1], v[38:39], v[2:3]
	s_nop 0
	v_pk_fma_f32 v[0:1], v[0:1], s[44:45], v[44:45] op_sel_hi:[1,0,0]
	s_nop 0
	v_mul_f32_e32 v2, 0x4b800000, v0
	v_cmp_gt_f32_e32 vcc, s83, v0
	s_nop 1
	v_cndmask_b32_e32 v0, v0, v2, vcc
	v_rsq_f32_e32 v0, v0
	v_bfe_u32 v2, v8, 16, 1
	v_add3_u32 v2, v8, v2, s84
	ds_write_b16_d16_hi v58, v2 offset:4416
	v_mul_f32_e32 v2, 0x45800000, v0
	v_cndmask_b32_e32 v0, v0, v2, vcc
	v_mul_f32_e32 v2, v10, v0
	v_bfe_u32 v3, v2, 16, 1
	v_add3_u32 v2, v2, v3, s84
	ds_write_b16_d16_hi v58, v2 offset:4608
	v_mul_f32_e32 v2, 0x4b800000, v1
	v_cmp_gt_f32_e32 vcc, s83, v1
	v_mul_f32_e32 v0, v26, v0
	s_nop 0
	v_cndmask_b32_e32 v1, v1, v2, vcc
	v_rsq_f32_e32 v1, v1
	v_bfe_u32 v2, v0, 16, 1
	v_add3_u32 v0, v0, v2, s84
	ds_write_b16_d16_hi v58, v0 offset:4672
	v_mul_f32_e32 v0, 0x45800000, v1
	v_cndmask_b32_e32 v0, v1, v0, vcc
	v_mul_f32_e32 v1, v11, v0
	v_bfe_u32 v2, v1, 16, 1
	v_add3_u32 v1, v1, v2, s84
	v_mul_f32_e32 v0, v27, v0
	ds_write_b16_d16_hi v58, v1 offset:4864
	v_bfe_u32 v1, v0, 16, 1
	v_add3_u32 v2, v0, v1, s84
	s_waitcnt lgkmcnt(8)
	v_pk_add_f32 v[0:1], v[32:33], v[4:5]
	ds_write_b16_d16_hi v58, v2 offset:4928
	v_pk_fma_f32 v[0:1], v[0:1], s[44:45], v[44:45] op_sel_hi:[1,0,0]
	v_lshlrev_b32_e32 v2, 8, v18
	v_mul_f32_e32 v3, 0x4b800000, v0
	v_cmp_gt_f32_e32 vcc, s83, v0
	v_add3_u32 v2, s8, v2, v59
	s_nop 0
	v_cndmask_b32_e32 v0, v0, v3, vcc
	v_rsq_f32_e32 v0, v0
	s_nop 0
	v_mul_f32_e32 v3, 0x45800000, v0
	v_cndmask_b32_e32 v0, v0, v3, vcc
	v_mul_f32_e32 v3, v12, v0
	v_bfe_u32 v4, v3, 16, 1
	v_add3_u32 v3, v3, v4, s84
	ds_write_b16_d16_hi v2, v3
	v_mul_f32_e32 v3, 0x4b800000, v1
	v_cmp_gt_f32_e32 vcc, s83, v1
	v_mul_f32_e32 v0, v28, v0
	s_nop 0
	v_cndmask_b32_e32 v1, v1, v3, vcc
	v_rsq_f32_e32 v1, v1
	v_bfe_u32 v3, v0, 16, 1
	v_add3_u32 v0, v0, v3, s84
	ds_write_b16_d16_hi v2, v0 offset:64
	v_mul_f32_e32 v0, 0x45800000, v1
	v_cndmask_b32_e32 v0, v1, v0, vcc
	v_mul_f32_e32 v1, v13, v0
	v_bfe_u32 v2, v1, 16, 1
	v_add3_u32 v1, v1, v2, s84
	ds_write_b16_d16_hi v58, v1 offset:6400
	v_mul_f32_e32 v2, v29, v0
	v_pk_add_f32 v[0:1], v[34:35], v[6:7]
	s_nop 0
	v_pk_fma_f32 v[0:1], v[0:1], s[44:45], v[44:45] op_sel_hi:[1,0,0]
	s_nop 0
	v_mul_f32_e32 v3, 0x4b800000, v0
	v_cmp_gt_f32_e32 vcc, s83, v0
	s_nop 1
	v_cndmask_b32_e32 v0, v0, v3, vcc
	v_rsq_f32_e32 v0, v0
	v_bfe_u32 v3, v2, 16, 1
	v_add3_u32 v2, v2, v3, s84
	ds_write_b16_d16_hi v58, v2 offset:6464
	v_mul_f32_e32 v2, 0x45800000, v0
	v_cndmask_b32_e32 v0, v0, v2, vcc
	v_mul_f32_e32 v2, v14, v0
	v_bfe_u32 v3, v2, 16, 1
	v_add3_u32 v2, v2, v3, s84
	ds_write_b16_d16_hi v58, v2 offset:6656
	v_mul_f32_e32 v2, 0x4b800000, v1
	v_cmp_gt_f32_e32 vcc, s83, v1
	v_mul_f32_e32 v0, v30, v0
	s_nop 0
	v_cndmask_b32_e32 v1, v1, v2, vcc
	v_rsq_f32_e32 v1, v1
	v_bfe_u32 v2, v0, 16, 1
	v_add3_u32 v0, v0, v2, s84
	ds_write_b16_d16_hi v58, v0 offset:6720
	v_mul_f32_e32 v0, 0x45800000, v1
	v_cndmask_b32_e32 v0, v1, v0, vcc
	v_mul_f32_e32 v1, v15, v0
	v_bfe_u32 v2, v1, 16, 1
	v_add3_u32 v1, v1, v2, s84
	v_mul_f32_e32 v0, v31, v0
	ds_write_b16_d16_hi v58, v1 offset:6912
	v_bfe_u32 v1, v0, 16, 1
	v_add3_u32 v0, v0, v1, s84
	v_cmp_gt_i32_e32 vcc, s85, v158
	ds_write_b16_d16_hi v58, v0 offset:6976
	s_waitcnt lgkmcnt(0)
	s_barrier
	s_and_saveexec_b64 s[48:49], vcc
	s_cbranch_execz .LBB0_651
	s_lshl_b64 s[6:7], s[40:41], 2
	s_add_u32 s4, s4, s6
	s_addc_u32 s5, s5, s7
	s_add_u32 s6, s65, s89
	s_addc_u32 s7, s66, 0
	s_add_u32 s6, s6, s40
	v_and_b32_e32 v2, 15, v158
	s_addc_u32 s7, s7, 0
	v_lshlrev_b32_e32 v0, 4, v2
	v_lshlrev_b32_e32 v156, 3, v2
	v_mov_b32_e32 v1, v157
	v_lshlrev_b32_e32 v2, 5, v2
	v_mov_b32_e32 v3, v157
	v_add_u32_e32 v8, 0, v0
	v_lshl_add_u64 v[0:1], v[160:161], 0, v[0:1]
	v_lshl_add_u64 v[2:3], s[4:5], 0, v[2:3]
	v_lshl_add_u64 v[4:5], s[6:7], 0, v[156:157]
	s_mov_b64 s[50:51], 0
	s_mov_b32 s98, 0xbfb8aa3b
	s_mov_b32 s100, 0x41800000
	v_ashrrev_i32_e32 v6, 4, v158
	global_load_dwordx4 v[36:39], v[2:3], off offset:16
	global_load_dwordx4 v[32:35], v[2:3], off
	v_mad_i64_i32 v[18:19], s[4:5], v6, s71, v[0:1]
	global_load_dwordx4 v[40:43], v[18:19], off offset:3072
	v_add_u32_e32 v9, 32, v6
	v_mad_i64_i32 v[20:21], s[4:5], v9, s71, v[0:1]
	global_load_dwordx4 v[44:47], v[20:21], off offset:3072
	v_add_u32_e32 v9, 64, v6
	v_mad_i64_i32 v[18:19], s[4:5], v9, s71, v[0:1]
	global_load_dwordx4 v[48:51], v[18:19], off offset:3072
	v_add_u32_e32 v9, 96, v6
	v_mad_i64_i32 v[20:21], s[4:5], v9, s71, v[0:1]
	global_load_dwordx4 v[52:55], v[20:21], off offset:3072
	v_lshl_add_u32 v7, v6, 8, v8
	ds_read_b128 v[22:25], v7
	s_waitcnt vmcnt(3) lgkmcnt(0)
; #define LAS __attribute__((address_space(3)))
; __device__ __forceinline__ float sigmoidf_(float x) { return 1.f / (1.f + __expf(-x)); }
; __device__ __forceinline__ unsigned pk4_fp8c(float a, float b, float c, float d) { return pk4_fp8(__builtin_amdgcn_fmed3f(a, -448.f, 448.f), __builtin_amdgcn_fmed3f(b, -448.f, 448.f), __builtin_amdgcn_fmed3f(c, -448.f, 448.f), __builtin_amdgcn_fmed3f(d, -448.f, 448.f)); }
; __device__ __forceinline__ void out_unit_m(LAS unsigned char* lds, LAS unsigned char* ldstab, const OutArgs a, const int wv) {
;     ...
; #pragma unroll 1
;     for (int id = tid; id < 128 * 16; id += 512) { const int row = id >> 4, ch = id & 15;
;         const u32x4 y = *(const LAS u32x4*)(lds + row * TP + ch * 16); const u32x4 g = *(const u32x4*)(a.G + (size_t)row * a.ldg + 8 * ch);
;         const f32x4 g0 = *(const f32x4*)(a.gain + 8 * ch), g1 = *(const f32x4*)(a.gain + 8 * ch + 4);
;         const float yv[8] = {bf_lo(y.x), bf_hi(y.x), bf_lo(y.y), bf_hi(y.y), bf_lo(y.z), bf_hi(y.z), bf_lo(y.w), bf_hi(y.w)};
;         const float gv[8] = {bf_lo(g.x), bf_hi(g.x), bf_lo(g.y), bf_hi(g.y), bf_lo(g.z), bf_hi(g.z), bf_lo(g.w), bf_hi(g.w)};
;         const float gn[8] = {g0[0], g0[1], g0[2], g0[3], g1[0], g1[1], g1[2], g1[3]};
;         float ov[8];
; #pragma unroll
;         for (int i = 0; i < 8; ++i) ov[i] = yv[i] * gn[i] * sigmoidf_(gv[i]);
;         u32x2 w; w.x = pg8::pk4_fp8c(ov[0] * a.oscale, ov[1] * a.oscale, ov[2] * a.oscale, ov[3] * a.oscale); w.y = pg8::pk4_fp8c(ov[4] * a.oscale, ov[5] * a.oscale, ov[6] * a.oscale, ov[7] * a.oscale);
;         *(u32x2*)(a.Out + (size_t)row * a.ldo + 8 * ch) = w; }
	v_lshlrev_b32_e32 v10, 16, v22
	v_and_b32_e32 v11, 0xffff0000, v22
	v_lshlrev_b32_e32 v12, 16, v23
	v_and_b32_e32 v13, 0xffff0000, v23
	v_lshlrev_b32_e32 v14, 16, v24
	v_and_b32_e32 v15, 0xffff0000, v24
	v_lshlrev_b32_e32 v16, 16, v25
	v_and_b32_e32 v17, 0xffff0000, v25
	v_pk_mul_f32 v[10:11], v[32:33], v[10:11]
	v_pk_mul_f32 v[12:13], v[34:35], v[12:13]
	v_pk_mul_f32 v[14:15], v[36:37], v[14:15]
	v_pk_mul_f32 v[16:17], v[38:39], v[16:17]
	v_lshlrev_b32_e32 v56, 16, v40
	v_and_b32_e32 v57, 0xffff0000, v40
	v_lshlrev_b32_e32 v58, 16, v41
	v_and_b32_e32 v59, 0xffff0000, v41
	v_pk_mul_f32 v[56:57], v[56:57], s[98:99] op_sel_hi:[1,0]
	v_pk_mul_f32 v[58:59], v[58:59], s[98:99] op_sel_hi:[1,0]
	v_exp_f32_e32 v56, v56
	v_exp_f32_e32 v57, v57
	v_exp_f32_e32 v58, v58
	v_exp_f32_e32 v59, v59
	v_pk_add_f32 v[56:57], v[56:57], 1.0 op_sel_hi:[1,0]
	v_pk_add_f32 v[58:59], v[58:59], 1.0 op_sel_hi:[1,0]
	v_rcp_f32_e32 v60, v56
	v_rcp_f32_e32 v61, v57
	v_rcp_f32_e32 v62, v58
	v_rcp_f32_e32 v63, v59
	v_pk_fma_f32 v[28:29], v[56:57], v[60:61], 1.0 op_sel_hi:[1,1,0] neg_lo:[1,0,0] neg_hi:[1,0,0]
	v_pk_fma_f32 v[30:31], v[58:59], v[62:63], 1.0 op_sel_hi:[1,1,0] neg_lo:[1,0,0] neg_hi:[1,0,0]
	s_nop 0
	v_pk_fma_f32 v[60:61], v[28:29], v[60:61], v[60:61]
	v_pk_fma_f32 v[62:63], v[30:31], v[62:63], v[62:63]
	s_nop 0
	v_pk_fma_f32 v[28:29], v[56:57], v[60:61], 1.0 op_sel_hi:[1,1,0] neg_lo:[1,0,0] neg_hi:[1,0,0]
	v_pk_fma_f32 v[30:31], v[58:59], v[62:63], 1.0 op_sel_hi:[1,1,0] neg_lo:[1,0,0] neg_hi:[1,0,0]
	s_nop 0
	v_pk_fma_f32 v[64:65], v[28:29], v[60:61], v[60:61]
	v_pk_fma_f32 v[66:67], v[30:31], v[62:63], v[62:63]
	s_nop 0
	v_pk_fma_f32 v[28:29], v[56:57], v[64:65], 1.0 op_sel_hi:[1,1,0] neg_lo:[1,0,0] neg_hi:[1,0,0]
	v_pk_fma_f32 v[30:31], v[58:59], v[66:67], 1.0 op_sel_hi:[1,1,0] neg_lo:[1,0,0] neg_hi:[1,0,0]
	s_nop 0
	v_pk_fma_f32 v[28:29], v[28:29], v[60:61], v[64:65]
	v_pk_fma_f32 v[30:31], v[30:31], v[62:63], v[66:67]
	v_div_fixup_f32 v28, v28, v56, 1.0
	v_div_fixup_f32 v29, v29, v57, 1.0
	v_div_fixup_f32 v30, v30, v58, 1.0
	v_div_fixup_f32 v31, v31, v59, 1.0
	v_pk_mul_f32 v[10:11], v[10:11], v[28:29]
	v_pk_mul_f32 v[12:13], v[12:13], v[30:31]
	v_lshlrev_b32_e32 v56, 16, v42
	v_and_b32_e32 v57, 0xffff0000, v42
	v_lshlrev_b32_e32 v58, 16, v43
	v_and_b32_e32 v59, 0xffff0000, v43
	v_pk_mul_f32 v[56:57], v[56:57], s[98:99] op_sel_hi:[1,0]
	v_pk_mul_f32 v[58:59], v[58:59], s[98:99] op_sel_hi:[1,0]
	v_exp_f32_e32 v56, v56
	v_exp_f32_e32 v57, v57
	v_exp_f32_e32 v58, v58
	v_exp_f32_e32 v59, v59
	v_pk_add_f32 v[56:57], v[56:57], 1.0 op_sel_hi:[1,0]
	v_pk_add_f32 v[58:59], v[58:59], 1.0 op_sel_hi:[1,0]
	v_rcp_f32_e32 v60, v56
	v_rcp_f32_e32 v61, v57
	v_rcp_f32_e32 v62, v58
	v_rcp_f32_e32 v63, v59
	v_pk_fma_f32 v[28:29], v[56:57], v[60:61], 1.0 op_sel_hi:[1,1,0] neg_lo:[1,0,0] neg_hi:[1,0,0]
	v_pk_fma_f32 v[30:31], v[58:59], v[62:63], 1.0 op_sel_hi:[1,1,0] neg_lo:[1,0,0] neg_hi:[1,0,0]
	s_nop 0
	v_pk_fma_f32 v[60:61], v[28:29], v[60:61], v[60:61]
	v_pk_fma_f32 v[62:63], v[30:31], v[62:63], v[62:63]
	s_nop 0
	v_pk_fma_f32 v[28:29], v[56:57], v[60:61], 1.0 op_sel_hi:[1,1,0] neg_lo:[1,0,0] neg_hi:[1,0,0]
	v_pk_fma_f32 v[30:31], v[58:59], v[62:63], 1.0 op_sel_hi:[1,1,0] neg_lo:[1,0,0] neg_hi:[1,0,0]
	s_nop 0
	v_pk_fma_f32 v[64:65], v[28:29], v[60:61], v[60:61]
	v_pk_fma_f32 v[66:67], v[30:31], v[62:63], v[62:63]
	s_nop 0
	v_pk_fma_f32 v[28:29], v[56:57], v[64:65], 1.0 op_sel_hi:[1,1,0] neg_lo:[1,0,0] neg_hi:[1,0,0]
	v_pk_fma_f32 v[30:31], v[58:59], v[66:67], 1.0 op_sel_hi:[1,1,0] neg_lo:[1,0,0] neg_hi:[1,0,0]
	s_nop 0
	v_pk_fma_f32 v[28:29], v[28:29], v[60:61], v[64:65]
	v_pk_fma_f32 v[30:31], v[30:31], v[62:63], v[66:67]
	v_div_fixup_f32 v28, v28, v56, 1.0
	v_div_fixup_f32 v29, v29, v57, 1.0
	v_div_fixup_f32 v30, v30, v58, 1.0
	v_div_fixup_f32 v31, v31, v59, 1.0
	v_pk_mul_f32 v[14:15], v[14:15], v[28:29]
	v_pk_mul_f32 v[16:17], v[16:17], v[30:31]
	v_pk_mul_f32 v[10:11], v[10:11], s[100:101] op_sel_hi:[1,0]
	v_pk_mul_f32 v[12:13], v[12:13], s[100:101] op_sel_hi:[1,0]
	v_pk_mul_f32 v[14:15], v[14:15], s[100:101] op_sel_hi:[1,0]
	v_pk_mul_f32 v[16:17], v[16:17], s[100:101] op_sel_hi:[1,0]
	v_med3_f32 v10, v10, s86, v202
	v_med3_f32 v11, v11, s86, v202
	v_med3_f32 v12, v12, s86, v202
	v_med3_f32 v13, v13, s86, v202
	v_med3_f32 v14, v14, s86, v202
	v_med3_f32 v15, v15, s86, v202
	v_med3_f32 v16, v16, s86, v202
	v_med3_f32 v17, v17, s86, v202
	v_mov_b32_e32 v20, v6
	v_mov_b32_e32 v21, 0
	v_cvt_pk_fp8_f32 v26, v10, v11
	v_cvt_pk_fp8_f32 v27, v14, v15
	v_lshlrev_b64 v[20:21], 10, v[20:21]
	v_cvt_pk_fp8_f32 v26, v12, v13 op_sel:[0,0,1]
	v_cvt_pk_fp8_f32 v27, v16, v17 op_sel:[0,0,1]
	v_lshl_add_u64 v[20:21], v[4:5], 0, v[20:21]
	s_nop 0
	global_store_dwordx2 v[20:21], v[26:27], off
	v_add_u32_e32 v9, 32, v6
	v_lshl_add_u32 v7, v9, 8, v8
	ds_read_b128 v[22:25], v7
	s_waitcnt vmcnt(3) lgkmcnt(0)
; #define LAS __attribute__((address_space(3)))
; __device__ __forceinline__ float sigmoidf_(float x) { return 1.f / (1.f + __expf(-x)); }
; __device__ __forceinline__ unsigned pk4_fp8c(float a, float b, float c, float d) { return pk4_fp8(__builtin_amdgcn_fmed3f(a, -448.f, 448.f), __builtin_amdgcn_fmed3f(b, -448.f, 448.f), __builtin_amdgcn_fmed3f(c, -448.f, 448.f), __builtin_amdgcn_fmed3f(d, -448.f, 448.f)); }
; __device__ __forceinline__ void out_unit_m(LAS unsigned char* lds, LAS unsigned char* ldstab, const OutArgs a, const int wv) {
;     ...
; #pragma unroll 1
;     for (int id = tid; id < 128 * 16; id += 512) { const int row = id >> 4, ch = id & 15;
;         const u32x4 y = *(const LAS u32x4*)(lds + row * TP + ch * 16); const u32x4 g = *(const u32x4*)(a.G + (size_t)row * a.ldg + 8 * ch);
;         const f32x4 g0 = *(const f32x4*)(a.gain + 8 * ch), g1 = *(const f32x4*)(a.gain + 8 * ch + 4);
;         const float yv[8] = {bf_lo(y.x), bf_hi(y.x), bf_lo(y.y), bf_hi(y.y), bf_lo(y.z), bf_hi(y.z), bf_lo(y.w), bf_hi(y.w)};
;         const float gv[8] = {bf_lo(g.x), bf_hi(g.x), bf_lo(g.y), bf_hi(g.y), bf_lo(g.z), bf_hi(g.z), bf_lo(g.w), bf_hi(g.w)};
;         const float gn[8] = {g0[0], g0[1], g0[2], g0[3], g1[0], g1[1], g1[2], g1[3]};
;         float ov[8];
; #pragma unroll
;         for (int i = 0; i < 8; ++i) ov[i] = yv[i] * gn[i] * sigmoidf_(gv[i]);
;         u32x2 w; w.x = pg8::pk4_fp8c(ov[0] * a.oscale, ov[1] * a.oscale, ov[2] * a.oscale, ov[3] * a.oscale); w.y = pg8::pk4_fp8c(ov[4] * a.oscale, ov[5] * a.oscale, ov[6] * a.oscale, ov[7] * a.oscale);
;         *(u32x2*)(a.Out + (size_t)row * a.ldo + 8 * ch) = w; }
	v_lshlrev_b32_e32 v10, 16, v22
	v_and_b32_e32 v11, 0xffff0000, v22
	v_lshlrev_b32_e32 v12, 16, v23
	v_and_b32_e32 v13, 0xffff0000, v23
	v_lshlrev_b32_e32 v14, 16, v24
	v_and_b32_e32 v15, 0xffff0000, v24
	v_lshlrev_b32_e32 v16, 16, v25
	v_and_b32_e32 v17, 0xffff0000, v25
	v_pk_mul_f32 v[10:11], v[32:33], v[10:11]
	v_pk_mul_f32 v[12:13], v[34:35], v[12:13]
	v_pk_mul_f32 v[14:15], v[36:37], v[14:15]
	v_pk_mul_f32 v[16:17], v[38:39], v[16:17]
	v_lshlrev_b32_e32 v56, 16, v44
	v_and_b32_e32 v57, 0xffff0000, v44
	v_lshlrev_b32_e32 v58, 16, v45
	v_and_b32_e32 v59, 0xffff0000, v45
	v_pk_mul_f32 v[56:57], v[56:57], s[98:99] op_sel_hi:[1,0]
	v_pk_mul_f32 v[58:59], v[58:59], s[98:99] op_sel_hi:[1,0]
	v_exp_f32_e32 v56, v56
	v_exp_f32_e32 v57, v57
	v_exp_f32_e32 v58, v58
	v_exp_f32_e32 v59, v59
	v_pk_add_f32 v[56:57], v[56:57], 1.0 op_sel_hi:[1,0]
	v_pk_add_f32 v[58:59], v[58:59], 1.0 op_sel_hi:[1,0]
	v_rcp_f32_e32 v60, v56
	v_rcp_f32_e32 v61, v57
	v_rcp_f32_e32 v62, v58
	v_rcp_f32_e32 v63, v59
	v_pk_fma_f32 v[28:29], v[56:57], v[60:61], 1.0 op_sel_hi:[1,1,0] neg_lo:[1,0,0] neg_hi:[1,0,0]
	v_pk_fma_f32 v[30:31], v[58:59], v[62:63], 1.0 op_sel_hi:[1,1,0] neg_lo:[1,0,0] neg_hi:[1,0,0]
	s_nop 0
	v_pk_fma_f32 v[60:61], v[28:29], v[60:61], v[60:61]
	v_pk_fma_f32 v[62:63], v[30:31], v[62:63], v[62:63]
	s_nop 0
	v_pk_fma_f32 v[28:29], v[56:57], v[60:61], 1.0 op_sel_hi:[1,1,0] neg_lo:[1,0,0] neg_hi:[1,0,0]
	v_pk_fma_f32 v[30:31], v[58:59], v[62:63], 1.0 op_sel_hi:[1,1,0] neg_lo:[1,0,0] neg_hi:[1,0,0]
	s_nop 0
	v_pk_fma_f32 v[64:65], v[28:29], v[60:61], v[60:61]
	v_pk_fma_f32 v[66:67], v[30:31], v[62:63], v[62:63]
	s_nop 0
	v_pk_fma_f32 v[28:29], v[56:57], v[64:65], 1.0 op_sel_hi:[1,1,0] neg_lo:[1,0,0] neg_hi:[1,0,0]
	v_pk_fma_f32 v[30:31], v[58:59], v[66:67], 1.0 op_sel_hi:[1,1,0] neg_lo:[1,0,0] neg_hi:[1,0,0]
	s_nop 0
	v_pk_fma_f32 v[28:29], v[28:29], v[60:61], v[64:65]
	v_pk_fma_f32 v[30:31], v[30:31], v[62:63], v[66:67]
	v_div_fixup_f32 v28, v28, v56, 1.0
	v_div_fixup_f32 v29, v29, v57, 1.0
	v_div_fixup_f32 v30, v30, v58, 1.0
	v_div_fixup_f32 v31, v31, v59, 1.0
	v_pk_mul_f32 v[10:11], v[10:11], v[28:29]
	v_pk_mul_f32 v[12:13], v[12:13], v[30:31]
	v_lshlrev_b32_e32 v56, 16, v46
	v_and_b32_e32 v57, 0xffff0000, v46
	v_lshlrev_b32_e32 v58, 16, v47
	v_and_b32_e32 v59, 0xffff0000, v47
	v_pk_mul_f32 v[56:57], v[56:57], s[98:99] op_sel_hi:[1,0]
	v_pk_mul_f32 v[58:59], v[58:59], s[98:99] op_sel_hi:[1,0]
	v_exp_f32_e32 v56, v56
	v_exp_f32_e32 v57, v57
	v_exp_f32_e32 v58, v58
	v_exp_f32_e32 v59, v59
	v_pk_add_f32 v[56:57], v[56:57], 1.0 op_sel_hi:[1,0]
	v_pk_add_f32 v[58:59], v[58:59], 1.0 op_sel_hi:[1,0]
	v_rcp_f32_e32 v60, v56
	v_rcp_f32_e32 v61, v57
	v_rcp_f32_e32 v62, v58
	v_rcp_f32_e32 v63, v59
	v_pk_fma_f32 v[28:29], v[56:57], v[60:61], 1.0 op_sel_hi:[1,1,0] neg_lo:[1,0,0] neg_hi:[1,0,0]
	v_pk_fma_f32 v[30:31], v[58:59], v[62:63], 1.0 op_sel_hi:[1,1,0] neg_lo:[1,0,0] neg_hi:[1,0,0]
	s_nop 0
	v_pk_fma_f32 v[60:61], v[28:29], v[60:61], v[60:61]
	v_pk_fma_f32 v[62:63], v[30:31], v[62:63], v[62:63]
	s_nop 0
	v_pk_fma_f32 v[28:29], v[56:57], v[60:61], 1.0 op_sel_hi:[1,1,0] neg_lo:[1,0,0] neg_hi:[1,0,0]
	v_pk_fma_f32 v[30:31], v[58:59], v[62:63], 1.0 op_sel_hi:[1,1,0] neg_lo:[1,0,0] neg_hi:[1,0,0]
	s_nop 0
	v_pk_fma_f32 v[64:65], v[28:29], v[60:61], v[60:61]
	v_pk_fma_f32 v[66:67], v[30:31], v[62:63], v[62:63]
	s_nop 0
	v_pk_fma_f32 v[28:29], v[56:57], v[64:65], 1.0 op_sel_hi:[1,1,0] neg_lo:[1,0,0] neg_hi:[1,0,0]
	v_pk_fma_f32 v[30:31], v[58:59], v[66:67], 1.0 op_sel_hi:[1,1,0] neg_lo:[1,0,0] neg_hi:[1,0,0]
	s_nop 0
	v_pk_fma_f32 v[28:29], v[28:29], v[60:61], v[64:65]
	v_pk_fma_f32 v[30:31], v[30:31], v[62:63], v[66:67]
	v_div_fixup_f32 v28, v28, v56, 1.0
	v_div_fixup_f32 v29, v29, v57, 1.0
	v_div_fixup_f32 v30, v30, v58, 1.0
	v_div_fixup_f32 v31, v31, v59, 1.0
	v_pk_mul_f32 v[14:15], v[14:15], v[28:29]
	v_pk_mul_f32 v[16:17], v[16:17], v[30:31]
	v_pk_mul_f32 v[10:11], v[10:11], s[100:101] op_sel_hi:[1,0]
	v_pk_mul_f32 v[12:13], v[12:13], s[100:101] op_sel_hi:[1,0]
	v_pk_mul_f32 v[14:15], v[14:15], s[100:101] op_sel_hi:[1,0]
	v_pk_mul_f32 v[16:17], v[16:17], s[100:101] op_sel_hi:[1,0]
	v_med3_f32 v10, v10, s86, v202
	v_med3_f32 v11, v11, s86, v202
	v_med3_f32 v12, v12, s86, v202
	v_med3_f32 v13, v13, s86, v202
	v_med3_f32 v14, v14, s86, v202
	v_med3_f32 v15, v15, s86, v202
	v_med3_f32 v16, v16, s86, v202
	v_med3_f32 v17, v17, s86, v202
	v_add_u32_e32 v20, 32, v6
	v_mov_b32_e32 v21, 0
	v_cvt_pk_fp8_f32 v26, v10, v11
	v_cvt_pk_fp8_f32 v27, v14, v15
	v_lshlrev_b64 v[20:21], 10, v[20:21]
	v_cvt_pk_fp8_f32 v26, v12, v13 op_sel:[0,0,1]
	v_cvt_pk_fp8_f32 v27, v16, v17 op_sel:[0,0,1]
	v_lshl_add_u64 v[20:21], v[4:5], 0, v[20:21]
	s_nop 0
	global_store_dwordx2 v[20:21], v[26:27], off
	v_add_u32_e32 v9, 64, v6
	v_lshl_add_u32 v7, v9, 8, v8
	ds_read_b128 v[22:25], v7
	s_waitcnt vmcnt(3) lgkmcnt(0)
; #define LAS __attribute__((address_space(3)))
; __device__ __forceinline__ float sigmoidf_(float x) { return 1.f / (1.f + __expf(-x)); }
; __device__ __forceinline__ unsigned pk4_fp8c(float a, float b, float c, float d) { return pk4_fp8(__builtin_amdgcn_fmed3f(a, -448.f, 448.f), __builtin_amdgcn_fmed3f(b, -448.f, 448.f), __builtin_amdgcn_fmed3f(c, -448.f, 448.f), __builtin_amdgcn_fmed3f(d, -448.f, 448.f)); }
; __device__ __forceinline__ void out_unit_m(LAS unsigned char* lds, LAS unsigned char* ldstab, const OutArgs a, const int wv) {
;     ...
; #pragma unroll 1
;     for (int id = tid; id < 128 * 16; id += 512) { const int row = id >> 4, ch = id & 15;
;         const u32x4 y = *(const LAS u32x4*)(lds + row * TP + ch * 16); const u32x4 g = *(const u32x4*)(a.G + (size_t)row * a.ldg + 8 * ch);
;         const f32x4 g0 = *(const f32x4*)(a.gain + 8 * ch), g1 = *(const f32x4*)(a.gain + 8 * ch + 4);
;         const float yv[8] = {bf_lo(y.x), bf_hi(y.x), bf_lo(y.y), bf_hi(y.y), bf_lo(y.z), bf_hi(y.z), bf_lo(y.w), bf_hi(y.w)};
;         const float gv[8] = {bf_lo(g.x), bf_hi(g.x), bf_lo(g.y), bf_hi(g.y), bf_lo(g.z), bf_hi(g.z), bf_lo(g.w), bf_hi(g.w)};
;         const float gn[8] = {g0[0], g0[1], g0[2], g0[3], g1[0], g1[1], g1[2], g1[3]};
;         float ov[8];
; #pragma unroll
;         for (int i = 0; i < 8; ++i) ov[i] = yv[i] * gn[i] * sigmoidf_(gv[i]);
;         u32x2 w; w.x = pg8::pk4_fp8c(ov[0] * a.oscale, ov[1] * a.oscale, ov[2] * a.oscale, ov[3] * a.oscale); w.y = pg8::pk4_fp8c(ov[4] * a.oscale, ov[5] * a.oscale, ov[6] * a.oscale, ov[7] * a.oscale);
;         *(u32x2*)(a.Out + (size_t)row * a.ldo + 8 * ch) = w; }
	v_lshlrev_b32_e32 v10, 16, v22
	v_and_b32_e32 v11, 0xffff0000, v22
	v_lshlrev_b32_e32 v12, 16, v23
	v_and_b32_e32 v13, 0xffff0000, v23
	v_lshlrev_b32_e32 v14, 16, v24
	v_and_b32_e32 v15, 0xffff0000, v24
	v_lshlrev_b32_e32 v16, 16, v25
	v_and_b32_e32 v17, 0xffff0000, v25
	v_pk_mul_f32 v[10:11], v[32:33], v[10:11]
	v_pk_mul_f32 v[12:13], v[34:35], v[12:13]
	v_pk_mul_f32 v[14:15], v[36:37], v[14:15]
	v_pk_mul_f32 v[16:17], v[38:39], v[16:17]
	v_lshlrev_b32_e32 v56, 16, v48
	v_and_b32_e32 v57, 0xffff0000, v48
	v_lshlrev_b32_e32 v58, 16, v49
	v_and_b32_e32 v59, 0xffff0000, v49
	v_pk_mul_f32 v[56:57], v[56:57], s[98:99] op_sel_hi:[1,0]
	v_pk_mul_f32 v[58:59], v[58:59], s[98:99] op_sel_hi:[1,0]
	v_exp_f32_e32 v56, v56
	v_exp_f32_e32 v57, v57
	v_exp_f32_e32 v58, v58
	v_exp_f32_e32 v59, v59
	v_pk_add_f32 v[56:57], v[56:57], 1.0 op_sel_hi:[1,0]
	v_pk_add_f32 v[58:59], v[58:59], 1.0 op_sel_hi:[1,0]
	v_rcp_f32_e32 v60, v56
	v_rcp_f32_e32 v61, v57
	v_rcp_f32_e32 v62, v58
	v_rcp_f32_e32 v63, v59
	v_pk_fma_f32 v[28:29], v[56:57], v[60:61], 1.0 op_sel_hi:[1,1,0] neg_lo:[1,0,0] neg_hi:[1,0,0]
	v_pk_fma_f32 v[30:31], v[58:59], v[62:63], 1.0 op_sel_hi:[1,1,0] neg_lo:[1,0,0] neg_hi:[1,0,0]
	s_nop 0
	v_pk_fma_f32 v[60:61], v[28:29], v[60:61], v[60:61]
	v_pk_fma_f32 v[62:63], v[30:31], v[62:63], v[62:63]
	s_nop 0
	v_pk_fma_f32 v[28:29], v[56:57], v[60:61], 1.0 op_sel_hi:[1,1,0] neg_lo:[1,0,0] neg_hi:[1,0,0]
	v_pk_fma_f32 v[30:31], v[58:59], v[62:63], 1.0 op_sel_hi:[1,1,0] neg_lo:[1,0,0] neg_hi:[1,0,0]
	s_nop 0
	v_pk_fma_f32 v[64:65], v[28:29], v[60:61], v[60:61]
	v_pk_fma_f32 v[66:67], v[30:31], v[62:63], v[62:63]
	s_nop 0
	v_pk_fma_f32 v[28:29], v[56:57], v[64:65], 1.0 op_sel_hi:[1,1,0] neg_lo:[1,0,0] neg_hi:[1,0,0]
	v_pk_fma_f32 v[30:31], v[58:59], v[66:67], 1.0 op_sel_hi:[1,1,0] neg_lo:[1,0,0] neg_hi:[1,0,0]
	s_nop 0
	v_pk_fma_f32 v[28:29], v[28:29], v[60:61], v[64:65]
	v_pk_fma_f32 v[30:31], v[30:31], v[62:63], v[66:67]
	v_div_fixup_f32 v28, v28, v56, 1.0
	v_div_fixup_f32 v29, v29, v57, 1.0
	v_div_fixup_f32 v30, v30, v58, 1.0
	v_div_fixup_f32 v31, v31, v59, 1.0
	v_pk_mul_f32 v[10:11], v[10:11], v[28:29]
	v_pk_mul_f32 v[12:13], v[12:13], v[30:31]
	v_lshlrev_b32_e32 v56, 16, v50
	v_and_b32_e32 v57, 0xffff0000, v50
	v_lshlrev_b32_e32 v58, 16, v51
	v_and_b32_e32 v59, 0xffff0000, v51
	v_pk_mul_f32 v[56:57], v[56:57], s[98:99] op_sel_hi:[1,0]
	v_pk_mul_f32 v[58:59], v[58:59], s[98:99] op_sel_hi:[1,0]
	v_exp_f32_e32 v56, v56
	v_exp_f32_e32 v57, v57
	v_exp_f32_e32 v58, v58
	v_exp_f32_e32 v59, v59
	v_pk_add_f32 v[56:57], v[56:57], 1.0 op_sel_hi:[1,0]
	v_pk_add_f32 v[58:59], v[58:59], 1.0 op_sel_hi:[1,0]
	v_rcp_f32_e32 v60, v56
	v_rcp_f32_e32 v61, v57
	v_rcp_f32_e32 v62, v58
	v_rcp_f32_e32 v63, v59
	v_pk_fma_f32 v[28:29], v[56:57], v[60:61], 1.0 op_sel_hi:[1,1,0] neg_lo:[1,0,0] neg_hi:[1,0,0]
	v_pk_fma_f32 v[30:31], v[58:59], v[62:63], 1.0 op_sel_hi:[1,1,0] neg_lo:[1,0,0] neg_hi:[1,0,0]
	s_nop 0
	v_pk_fma_f32 v[60:61], v[28:29], v[60:61], v[60:61]
	v_pk_fma_f32 v[62:63], v[30:31], v[62:63], v[62:63]
	s_nop 0
	v_pk_fma_f32 v[28:29], v[56:57], v[60:61], 1.0 op_sel_hi:[1,1,0] neg_lo:[1,0,0] neg_hi:[1,0,0]
	v_pk_fma_f32 v[30:31], v[58:59], v[62:63], 1.0 op_sel_hi:[1,1,0] neg_lo:[1,0,0] neg_hi:[1,0,0]
	s_nop 0
	v_pk_fma_f32 v[64:65], v[28:29], v[60:61], v[60:61]
	v_pk_fma_f32 v[66:67], v[30:31], v[62:63], v[62:63]
	s_nop 0
	v_pk_fma_f32 v[28:29], v[56:57], v[64:65], 1.0 op_sel_hi:[1,1,0] neg_lo:[1,0,0] neg_hi:[1,0,0]
	v_pk_fma_f32 v[30:31], v[58:59], v[66:67], 1.0 op_sel_hi:[1,1,0] neg_lo:[1,0,0] neg_hi:[1,0,0]
	s_nop 0
	v_pk_fma_f32 v[28:29], v[28:29], v[60:61], v[64:65]
	v_pk_fma_f32 v[30:31], v[30:31], v[62:63], v[66:67]
	v_div_fixup_f32 v28, v28, v56, 1.0
	v_div_fixup_f32 v29, v29, v57, 1.0
	v_div_fixup_f32 v30, v30, v58, 1.0
	v_div_fixup_f32 v31, v31, v59, 1.0
	v_pk_mul_f32 v[14:15], v[14:15], v[28:29]
	v_pk_mul_f32 v[16:17], v[16:17], v[30:31]
	v_pk_mul_f32 v[10:11], v[10:11], s[100:101] op_sel_hi:[1,0]
	v_pk_mul_f32 v[12:13], v[12:13], s[100:101] op_sel_hi:[1,0]
	v_pk_mul_f32 v[14:15], v[14:15], s[100:101] op_sel_hi:[1,0]
	v_pk_mul_f32 v[16:17], v[16:17], s[100:101] op_sel_hi:[1,0]
	v_med3_f32 v10, v10, s86, v202
	v_med3_f32 v11, v11, s86, v202
	v_med3_f32 v12, v12, s86, v202
	v_med3_f32 v13, v13, s86, v202
	v_med3_f32 v14, v14, s86, v202
	v_med3_f32 v15, v15, s86, v202
	v_med3_f32 v16, v16, s86, v202
	v_med3_f32 v17, v17, s86, v202
	v_add_u32_e32 v20, 64, v6
	v_mov_b32_e32 v21, 0
	v_cvt_pk_fp8_f32 v26, v10, v11
	v_cvt_pk_fp8_f32 v27, v14, v15
	v_lshlrev_b64 v[20:21], 10, v[20:21]
	v_cvt_pk_fp8_f32 v26, v12, v13 op_sel:[0,0,1]
	v_cvt_pk_fp8_f32 v27, v16, v17 op_sel:[0,0,1]
	v_lshl_add_u64 v[20:21], v[4:5], 0, v[20:21]
	s_nop 0
	global_store_dwordx2 v[20:21], v[26:27], off
	v_add_u32_e32 v9, 96, v6
	v_lshl_add_u32 v7, v9, 8, v8
	ds_read_b128 v[22:25], v7
	s_waitcnt vmcnt(3) lgkmcnt(0)
; #define LAS __attribute__((address_space(3)))
; __device__ __forceinline__ float sigmoidf_(float x) { return 1.f / (1.f + __expf(-x)); }
; __device__ __forceinline__ unsigned pk4_fp8c(float a, float b, float c, float d) { return pk4_fp8(__builtin_amdgcn_fmed3f(a, -448.f, 448.f), __builtin_amdgcn_fmed3f(b, -448.f, 448.f), __builtin_amdgcn_fmed3f(c, -448.f, 448.f), __builtin_amdgcn_fmed3f(d, -448.f, 448.f)); }
; __device__ __forceinline__ void out_unit_m(LAS unsigned char* lds, LAS unsigned char* ldstab, const OutArgs a, const int wv) {
;     ...
; #pragma unroll 1
;     for (int id = tid; id < 128 * 16; id += 512) { const int row = id >> 4, ch = id & 15;
;         const u32x4 y = *(const LAS u32x4*)(lds + row * TP + ch * 16); const u32x4 g = *(const u32x4*)(a.G + (size_t)row * a.ldg + 8 * ch);
;         const f32x4 g0 = *(const f32x4*)(a.gain + 8 * ch), g1 = *(const f32x4*)(a.gain + 8 * ch + 4);
;         const float yv[8] = {bf_lo(y.x), bf_hi(y.x), bf_lo(y.y), bf_hi(y.y), bf_lo(y.z), bf_hi(y.z), bf_lo(y.w), bf_hi(y.w)};
;         const float gv[8] = {bf_lo(g.x), bf_hi(g.x), bf_lo(g.y), bf_hi(g.y), bf_lo(g.z), bf_hi(g.z), bf_lo(g.w), bf_hi(g.w)};
;         const float gn[8] = {g0[0], g0[1], g0[2], g0[3], g1[0], g1[1], g1[2], g1[3]};
;         float ov[8];
; #pragma unroll
;         for (int i = 0; i < 8; ++i) ov[i] = yv[i] * gn[i] * sigmoidf_(gv[i]);
;         u32x2 w; w.x = pg8::pk4_fp8c(ov[0] * a.oscale, ov[1] * a.oscale, ov[2] * a.oscale, ov[3] * a.oscale); w.y = pg8::pk4_fp8c(ov[4] * a.oscale, ov[5] * a.oscale, ov[6] * a.oscale, ov[7] * a.oscale);
;         *(u32x2*)(a.Out + (size_t)row * a.ldo + 8 * ch) = w; }
	v_lshlrev_b32_e32 v10, 16, v22
	v_and_b32_e32 v11, 0xffff0000, v22
	v_lshlrev_b32_e32 v12, 16, v23
	v_and_b32_e32 v13, 0xffff0000, v23
	v_lshlrev_b32_e32 v14, 16, v24
	v_and_b32_e32 v15, 0xffff0000, v24
	v_lshlrev_b32_e32 v16, 16, v25
	v_and_b32_e32 v17, 0xffff0000, v25
	v_pk_mul_f32 v[10:11], v[32:33], v[10:11]
	v_pk_mul_f32 v[12:13], v[34:35], v[12:13]
	v_pk_mul_f32 v[14:15], v[36:37], v[14:15]
	v_pk_mul_f32 v[16:17], v[38:39], v[16:17]
	v_lshlrev_b32_e32 v56, 16, v52
	v_and_b32_e32 v57, 0xffff0000, v52
	v_lshlrev_b32_e32 v58, 16, v53
	v_and_b32_e32 v59, 0xffff0000, v53
	v_pk_mul_f32 v[56:57], v[56:57], s[98:99] op_sel_hi:[1,0]
	v_pk_mul_f32 v[58:59], v[58:59], s[98:99] op_sel_hi:[1,0]
	v_exp_f32_e32 v56, v56
	v_exp_f32_e32 v57, v57
	v_exp_f32_e32 v58, v58
	v_exp_f32_e32 v59, v59
	v_pk_add_f32 v[56:57], v[56:57], 1.0 op_sel_hi:[1,0]
	v_pk_add_f32 v[58:59], v[58:59], 1.0 op_sel_hi:[1,0]
	v_rcp_f32_e32 v60, v56
	v_rcp_f32_e32 v61, v57
	v_rcp_f32_e32 v62, v58
	v_rcp_f32_e32 v63, v59
	v_pk_fma_f32 v[28:29], v[56:57], v[60:61], 1.0 op_sel_hi:[1,1,0] neg_lo:[1,0,0] neg_hi:[1,0,0]
	v_pk_fma_f32 v[30:31], v[58:59], v[62:63], 1.0 op_sel_hi:[1,1,0] neg_lo:[1,0,0] neg_hi:[1,0,0]
	s_nop 0
	v_pk_fma_f32 v[60:61], v[28:29], v[60:61], v[60:61]
	v_pk_fma_f32 v[62:63], v[30:31], v[62:63], v[62:63]
	s_nop 0
	v_pk_fma_f32 v[28:29], v[56:57], v[60:61], 1.0 op_sel_hi:[1,1,0] neg_lo:[1,0,0] neg_hi:[1,0,0]
	v_pk_fma_f32 v[30:31], v[58:59], v[62:63], 1.0 op_sel_hi:[1,1,0] neg_lo:[1,0,0] neg_hi:[1,0,0]
	s_nop 0
	v_pk_fma_f32 v[64:65], v[28:29], v[60:61], v[60:61]
	v_pk_fma_f32 v[66:67], v[30:31], v[62:63], v[62:63]
	s_nop 0
	v_pk_fma_f32 v[28:29], v[56:57], v[64:65], 1.0 op_sel_hi:[1,1,0] neg_lo:[1,0,0] neg_hi:[1,0,0]
	v_pk_fma_f32 v[30:31], v[58:59], v[66:67], 1.0 op_sel_hi:[1,1,0] neg_lo:[1,0,0] neg_hi:[1,0,0]
	s_nop 0
	v_pk_fma_f32 v[28:29], v[28:29], v[60:61], v[64:65]
	v_pk_fma_f32 v[30:31], v[30:31], v[62:63], v[66:67]
	v_div_fixup_f32 v28, v28, v56, 1.0
	v_div_fixup_f32 v29, v29, v57, 1.0
	v_div_fixup_f32 v30, v30, v58, 1.0
	v_div_fixup_f32 v31, v31, v59, 1.0
	v_pk_mul_f32 v[10:11], v[10:11], v[28:29]
	v_pk_mul_f32 v[12:13], v[12:13], v[30:31]
	v_lshlrev_b32_e32 v56, 16, v54
	v_and_b32_e32 v57, 0xffff0000, v54
	v_lshlrev_b32_e32 v58, 16, v55
	v_and_b32_e32 v59, 0xffff0000, v55
	v_pk_mul_f32 v[56:57], v[56:57], s[98:99] op_sel_hi:[1,0]
	v_pk_mul_f32 v[58:59], v[58:59], s[98:99] op_sel_hi:[1,0]
	v_exp_f32_e32 v56, v56
	v_exp_f32_e32 v57, v57
	v_exp_f32_e32 v58, v58
	v_exp_f32_e32 v59, v59
	v_pk_add_f32 v[56:57], v[56:57], 1.0 op_sel_hi:[1,0]
	v_pk_add_f32 v[58:59], v[58:59], 1.0 op_sel_hi:[1,0]
	v_rcp_f32_e32 v60, v56
	v_rcp_f32_e32 v61, v57
	v_rcp_f32_e32 v62, v58
	v_rcp_f32_e32 v63, v59
	v_pk_fma_f32 v[28:29], v[56:57], v[60:61], 1.0 op_sel_hi:[1,1,0] neg_lo:[1,0,0] neg_hi:[1,0,0]
	v_pk_fma_f32 v[30:31], v[58:59], v[62:63], 1.0 op_sel_hi:[1,1,0] neg_lo:[1,0,0] neg_hi:[1,0,0]
	s_nop 0
	v_pk_fma_f32 v[60:61], v[28:29], v[60:61], v[60:61]
	v_pk_fma_f32 v[62:63], v[30:31], v[62:63], v[62:63]
	s_nop 0
	v_pk_fma_f32 v[28:29], v[56:57], v[60:61], 1.0 op_sel_hi:[1,1,0] neg_lo:[1,0,0] neg_hi:[1,0,0]
	v_pk_fma_f32 v[30:31], v[58:59], v[62:63], 1.0 op_sel_hi:[1,1,0] neg_lo:[1,0,0] neg_hi:[1,0,0]
	s_nop 0
	v_pk_fma_f32 v[64:65], v[28:29], v[60:61], v[60:61]
	v_pk_fma_f32 v[66:67], v[30:31], v[62:63], v[62:63]
	s_nop 0
	v_pk_fma_f32 v[28:29], v[56:57], v[64:65], 1.0 op_sel_hi:[1,1,0] neg_lo:[1,0,0] neg_hi:[1,0,0]
	v_pk_fma_f32 v[30:31], v[58:59], v[66:67], 1.0 op_sel_hi:[1,1,0] neg_lo:[1,0,0] neg_hi:[1,0,0]
	s_nop 0
	v_pk_fma_f32 v[28:29], v[28:29], v[60:61], v[64:65]
	v_pk_fma_f32 v[30:31], v[30:31], v[62:63], v[66:67]
	v_div_fixup_f32 v28, v28, v56, 1.0
	v_div_fixup_f32 v29, v29, v57, 1.0
	v_div_fixup_f32 v30, v30, v58, 1.0
	v_div_fixup_f32 v31, v31, v59, 1.0
	v_pk_mul_f32 v[14:15], v[14:15], v[28:29]
	v_pk_mul_f32 v[16:17], v[16:17], v[30:31]
	v_pk_mul_f32 v[10:11], v[10:11], s[100:101] op_sel_hi:[1,0]
	v_pk_mul_f32 v[12:13], v[12:13], s[100:101] op_sel_hi:[1,0]
	v_pk_mul_f32 v[14:15], v[14:15], s[100:101] op_sel_hi:[1,0]
	v_pk_mul_f32 v[16:17], v[16:17], s[100:101] op_sel_hi:[1,0]
	v_med3_f32 v10, v10, s86, v202
	v_med3_f32 v11, v11, s86, v202
	v_med3_f32 v12, v12, s86, v202
	v_med3_f32 v13, v13, s86, v202
	v_med3_f32 v14, v14, s86, v202
	v_med3_f32 v15, v15, s86, v202
	v_med3_f32 v16, v16, s86, v202
	v_med3_f32 v17, v17, s86, v202
	v_add_u32_e32 v20, 96, v6
	v_mov_b32_e32 v21, 0
	v_cvt_pk_fp8_f32 v26, v10, v11
	v_cvt_pk_fp8_f32 v27, v14, v15
	v_lshlrev_b64 v[20:21], 10, v[20:21]
	v_cvt_pk_fp8_f32 v26, v12, v13 op_sel:[0,0,1]
	v_cvt_pk_fp8_f32 v27, v16, v17 op_sel:[0,0,1]
	v_lshl_add_u64 v[20:21], v[4:5], 0, v[20:21]
	s_nop 0
	global_store_dwordx2 v[20:21], v[26:27], off

; #define LAS __attribute__((address_space(3)))
; __device__ __forceinline__ bf16_t f2bf(float f) { unsigned u = __builtin_bit_cast(unsigned, f); return (bf16_t)((u + 0x7fffu + ((u >> 16) & 1u)) >> 16); }
; __device__ __forceinline__ int crow(int r, int hi) { return (r & 3) + 8 * (r >> 2) + 4 * hi; }
; __device__ __forceinline__ int crow(int r, int hi) { return (r & 3) + 8 * (r >> 2) + 4 * hi; }
; __device__ __forceinline__ void out_unit_m(LAS unsigned char* lds, LAS unsigned char* ldstab, const OutArgs a, const int wv) {
;     ...
;     __syncthreads();
;     constexpr int TP = DV * 2;
; #pragma unroll
;     for (int r = 0; r < 16; ++r) { const int row = 32 * rb + crow(r, hi);
;         const float inv = rsqrtf((s2[r] + exch[(1 - dh) * 128 + row]) * (1.f / DV) + EPS);
; #pragma unroll
;         for (int nb = 0; nb < 2; ++nb) *(LAS bf16_t*)(lds + row * TP + (dh * 64 + 32 * nb + r32) * 2) = f2bf(o[nb][r] * inv); }
.LBB0_3189:
	s_or_b64 exec, exec, s[6:7]
	v_or_b32_e32 v56, s12, v156
	s_lshl_b32 s6, s8, 7
	v_subrev_u32_e32 v48, s6, v56
	s_add_i32 s7, 0, 0x22100
	v_lshl_add_u32 v48, v48, 2, s7
	s_waitcnt lgkmcnt(0)
	s_barrier
	ds_read_b128 v[48:51], v48 offset:512
	v_or_b32_e32 v57, 8, v56
	v_subrev_u32_e32 v52, s6, v57
	v_lshl_add_u32 v52, v52, 2, s7
	ds_read_b128 v[52:55], v52 offset:512
	s_waitcnt lgkmcnt(1)
	v_pk_add_f32 v[48:49], v[44:45], v[48:49]
	v_mov_b64_e32 v[44:45], s[46:47]
	v_pk_fma_f32 v[48:49], v[48:49], s[44:45], v[44:45] op_sel_hi:[1,0,0]
	v_lshlrev_b32_e32 v59, 1, v159
	v_mul_f32_e32 v58, 0x4b800000, v48
	v_cmp_gt_f32_e32 vcc, s83, v48
	s_add_i32 s8, s6, 0
	s_nop 0
	v_cndmask_b32_e32 v48, v48, v58, vcc
	v_rsq_f32_e32 v48, v48
	v_lshlrev_b32_e32 v58, 8, v56
	v_add3_u32 v58, s8, v58, v59
	v_mul_f32_e32 v60, 0x45800000, v48
	v_cndmask_b32_e32 v48, v48, v60, vcc
	v_mul_f32_e32 v0, v0, v48
	v_bfe_u32 v60, v0, 16, 1
	v_add3_u32 v0, v0, v60, s84
	ds_write_b16_d16_hi v58, v0
	v_mul_f32_e32 v0, v16, v48
	v_mul_f32_e32 v16, 0x4b800000, v49
	v_cmp_gt_f32_e32 vcc, s83, v49
	v_bfe_u32 v48, v0, 16, 1
	v_add3_u32 v0, v0, v48, s84
	v_cndmask_b32_e32 v16, v49, v16, vcc
	v_rsq_f32_e32 v16, v16
	ds_write_b16_d16_hi v58, v0 offset:64
	v_mul_f32_e32 v0, 0x45800000, v16
	v_cndmask_b32_e32 v0, v16, v0, vcc
	v_mul_f32_e32 v1, v1, v0
	v_bfe_u32 v16, v1, 16, 1
	v_add3_u32 v1, v1, v16, s84
	ds_write_b16_d16_hi v58, v1 offset:256
	v_mul_f32_e32 v16, v17, v0
	v_pk_add_f32 v[0:1], v[46:47], v[50:51]
	s_nop 0
	v_pk_fma_f32 v[0:1], v[0:1], s[44:45], v[44:45] op_sel_hi:[1,0,0]
	s_nop 0
	v_mul_f32_e32 v17, 0x4b800000, v0
	v_cmp_gt_f32_e32 vcc, s83, v0
	s_nop 1
	v_cndmask_b32_e32 v0, v0, v17, vcc
	v_rsq_f32_e32 v0, v0
	v_bfe_u32 v17, v16, 16, 1
	v_add3_u32 v16, v16, v17, s84
	ds_write_b16_d16_hi v58, v16 offset:320
	v_mul_f32_e32 v16, 0x45800000, v0
	v_cndmask_b32_e32 v0, v0, v16, vcc
	v_mul_f32_e32 v2, v2, v0
	v_bfe_u32 v16, v2, 16, 1
	v_add3_u32 v2, v2, v16, s84
	ds_write_b16_d16_hi v58, v2 offset:512
	v_mul_f32_e32 v2, 0x4b800000, v1
	v_cmp_gt_f32_e32 vcc, s83, v1
	v_mul_f32_e32 v0, v18, v0
	v_or_b32_e32 v17, 16, v56
	v_cndmask_b32_e32 v1, v1, v2, vcc
	v_rsq_f32_e32 v1, v1
	v_bfe_u32 v2, v0, 16, 1
	v_add3_u32 v0, v0, v2, s84
	ds_write_b16_d16_hi v58, v0 offset:576
	v_mul_f32_e32 v0, 0x45800000, v1
	v_cndmask_b32_e32 v0, v1, v0, vcc
	v_mul_f32_e32 v1, v3, v0
	v_bfe_u32 v2, v1, 16, 1
	v_add3_u32 v1, v1, v2, s84
	v_mul_f32_e32 v0, v19, v0
	ds_write_b16_d16_hi v58, v1 offset:768
	v_bfe_u32 v1, v0, 16, 1
	v_add3_u32 v2, v0, v1, s84
	s_waitcnt lgkmcnt(7)
	v_pk_add_f32 v[0:1], v[40:41], v[52:53]
	ds_write_b16_d16_hi v58, v2 offset:832
	v_pk_fma_f32 v[0:1], v[0:1], s[44:45], v[44:45] op_sel_hi:[1,0,0]
	v_lshlrev_b32_e32 v2, 8, v57
	v_mul_f32_e32 v3, 0x4b800000, v0
	v_cmp_gt_f32_e32 vcc, s83, v0
	v_add3_u32 v2, s8, v2, v59
	v_or_b32_e32 v18, 24, v56
	v_cndmask_b32_e32 v0, v0, v3, vcc
	v_rsq_f32_e32 v0, v0
	s_nop 0
	v_mul_f32_e32 v3, 0x45800000, v0
	v_cndmask_b32_e32 v0, v0, v3, vcc
	v_mul_f32_e32 v3, v4, v0
	v_bfe_u32 v4, v3, 16, 1
	v_add3_u32 v3, v3, v4, s84
	ds_write_b16_d16_hi v2, v3
	v_mul_f32_e32 v3, 0x4b800000, v1
	v_cmp_gt_f32_e32 vcc, s83, v1
	v_mul_f32_e32 v0, v20, v0
	v_subrev_u32_e32 v4, s6, v18
	v_cndmask_b32_e32 v1, v1, v3, vcc
	v_rsq_f32_e32 v1, v1
	v_bfe_u32 v3, v0, 16, 1
	v_add3_u32 v0, v0, v3, s84
	ds_write_b16_d16_hi v2, v0 offset:64
	v_mul_f32_e32 v0, 0x45800000, v1
	v_cndmask_b32_e32 v0, v1, v0, vcc
	v_mul_f32_e32 v1, v5, v0
	v_bfe_u32 v2, v1, 16, 1
	v_add3_u32 v1, v1, v2, s84
	ds_write_b16_d16_hi v58, v1 offset:2304
	v_mul_f32_e32 v2, v21, v0
	v_pk_add_f32 v[0:1], v[42:43], v[54:55]
	v_lshl_add_u32 v4, v4, 2, s7
	v_pk_fma_f32 v[0:1], v[0:1], s[44:45], v[44:45] op_sel_hi:[1,0,0]
	s_nop 0
	v_mul_f32_e32 v3, 0x4b800000, v0
	v_cmp_gt_f32_e32 vcc, s83, v0
	s_nop 1
	v_cndmask_b32_e32 v0, v0, v3, vcc
	v_rsq_f32_e32 v0, v0
	v_bfe_u32 v3, v2, 16, 1
	v_add3_u32 v2, v2, v3, s84
	ds_write_b16_d16_hi v58, v2 offset:2368
	v_mul_f32_e32 v2, 0x45800000, v0
	v_cndmask_b32_e32 v0, v0, v2, vcc
	v_mul_f32_e32 v2, v6, v0
	v_bfe_u32 v3, v2, 16, 1
	v_add3_u32 v2, v2, v3, s84
	ds_write_b16_d16_hi v58, v2 offset:2560
	v_mul_f32_e32 v2, 0x4b800000, v1
	v_cmp_gt_f32_e32 vcc, s83, v1
	v_mul_f32_e32 v0, v22, v0
	s_nop 0
	v_cndmask_b32_e32 v1, v1, v2, vcc
	v_rsq_f32_e32 v1, v1
	v_bfe_u32 v2, v0, 16, 1
	v_add3_u32 v0, v0, v2, s84
	ds_write_b16_d16_hi v58, v0 offset:2624
	v_mul_f32_e32 v0, 0x45800000, v1
	v_cndmask_b32_e32 v0, v1, v0, vcc
	v_mul_f32_e32 v1, v7, v0
	v_bfe_u32 v2, v1, 16, 1
	v_add3_u32 v1, v1, v2, s84
	v_mul_f32_e32 v0, v23, v0
	ds_write_b16_d16_hi v58, v1 offset:2816
	v_bfe_u32 v1, v0, 16, 1
	v_add3_u32 v16, v0, v1, s84
	v_subrev_u32_e32 v0, s6, v17
	v_lshl_add_u32 v0, v0, 2, s7
	ds_read_b128 v[0:3], v0 offset:512
	ds_read_b128 v[4:7], v4 offset:512
	ds_write_b16_d16_hi v58, v16 offset:2880
	v_lshlrev_b32_e32 v16, 8, v17
	v_add3_u32 v16, s8, v16, v59
	s_waitcnt lgkmcnt(2)
; #define LAS __attribute__((address_space(3)))
; __device__ __forceinline__ bf16_t f2bf(float f) { unsigned u = __builtin_bit_cast(unsigned, f); return (bf16_t)((u + 0x7fffu + ((u >> 16) & 1u)) >> 16); }
; __device__ __forceinline__ int crow(int r, int hi) { return (r & 3) + 8 * (r >> 2) + 4 * hi; }
; __device__ __forceinline__ int crow(int r, int hi) { return (r & 3) + 8 * (r >> 2) + 4 * hi; }
; __device__ __forceinline__ void out_unit_m(LAS unsigned char* lds, LAS unsigned char* ldstab, const OutArgs a, const int wv) {
;     ...
;     for (int r = 0; r < 16; ++r) { const int row = 32 * rb + crow(r, hi);
;         const float inv = rsqrtf((s2[r] + exch[(1 - dh) * 128 + row]) * (1.f / DV) + EPS);
; #pragma unroll
;         for (int nb = 0; nb < 2; ++nb) *(LAS bf16_t*)(lds + row * TP + (dh * 64 + 32 * nb + r32) * 2) = f2bf(o[nb][r] * inv); }
;     __syncthreads();
; #pragma unroll 1
;     for (int id = tid; id < 128 * 16; id += 512) { const int row = id >> 4, ch = id & 15;
;         const u32x4 y = *(const LAS u32x4*)(lds + row * TP + ch * 16); const u32x4 g = *(const u32x4*)(a.G + (size_t)row * a.ldg + 8 * ch);
	v_pk_add_f32 v[0:1], v[36:37], v[0:1]
	s_nop 0
	v_pk_fma_f32 v[0:1], v[0:1], s[44:45], v[44:45] op_sel_hi:[1,0,0]
	s_nop 0
	v_mul_f32_e32 v19, 0x4b800000, v0
	v_cmp_gt_f32_e32 vcc, s83, v0
	s_nop 1
	v_cndmask_b32_e32 v0, v0, v19, vcc
	v_rsq_f32_e32 v0, v0
	s_nop 0
	v_mul_f32_e32 v17, 0x45800000, v0
	v_cndmask_b32_e32 v0, v0, v17, vcc
	v_mul_f32_e32 v8, v8, v0
	v_bfe_u32 v17, v8, 16, 1
	v_add3_u32 v8, v8, v17, s84
	ds_write_b16_d16_hi v16, v8
	v_mul_f32_e32 v8, 0x4b800000, v1
	v_cmp_gt_f32_e32 vcc, s83, v1
	v_mul_f32_e32 v0, v24, v0
	s_nop 0
	v_cndmask_b32_e32 v1, v1, v8, vcc
	v_rsq_f32_e32 v1, v1
	v_bfe_u32 v8, v0, 16, 1
	v_add3_u32 v0, v0, v8, s84
	ds_write_b16_d16_hi v16, v0 offset:64
	v_mul_f32_e32 v0, 0x45800000, v1
	v_cndmask_b32_e32 v0, v1, v0, vcc
	v_mul_f32_e32 v1, v9, v0
	v_bfe_u32 v8, v1, 16, 1
	v_add3_u32 v1, v1, v8, s84
	ds_write_b16_d16_hi v58, v1 offset:4352
	v_mul_f32_e32 v8, v25, v0
	v_pk_add_f32 v[0:1], v[38:39], v[2:3]
	s_nop 0
	v_pk_fma_f32 v[0:1], v[0:1], s[44:45], v[44:45] op_sel_hi:[1,0,0]
	s_nop 0
	v_mul_f32_e32 v2, 0x4b800000, v0
	v_cmp_gt_f32_e32 vcc, s83, v0
	s_nop 1
	v_cndmask_b32_e32 v0, v0, v2, vcc
	v_rsq_f32_e32 v0, v0
	v_bfe_u32 v2, v8, 16, 1
	v_add3_u32 v2, v8, v2, s84
	ds_write_b16_d16_hi v58, v2 offset:4416
	v_mul_f32_e32 v2, 0x45800000, v0
	v_cndmask_b32_e32 v0, v0, v2, vcc
	v_mul_f32_e32 v2, v10, v0
	v_bfe_u32 v3, v2, 16, 1
	v_add3_u32 v2, v2, v3, s84
	ds_write_b16_d16_hi v58, v2 offset:4608
	v_mul_f32_e32 v2, 0x4b800000, v1
	v_cmp_gt_f32_e32 vcc, s83, v1
	v_mul_f32_e32 v0, v26, v0
	s_nop 0
	v_cndmask_b32_e32 v1, v1, v2, vcc
	v_rsq_f32_e32 v1, v1
	v_bfe_u32 v2, v0, 16, 1
	v_add3_u32 v0, v0, v2, s84
	ds_write_b16_d16_hi v58, v0 offset:4672
	v_mul_f32_e32 v0, 0x45800000, v1
	v_cndmask_b32_e32 v0, v1, v0, vcc
	v_mul_f32_e32 v1, v11, v0
	v_bfe_u32 v2, v1, 16, 1
	v_add3_u32 v1, v1, v2, s84
	v_mul_f32_e32 v0, v27, v0
	ds_write_b16_d16_hi v58, v1 offset:4864
	v_bfe_u32 v1, v0, 16, 1
	v_add3_u32 v2, v0, v1, s84
	s_waitcnt lgkmcnt(8)
	v_pk_add_f32 v[0:1], v[32:33], v[4:5]
	ds_write_b16_d16_hi v58, v2 offset:4928
	v_pk_fma_f32 v[0:1], v[0:1], s[44:45], v[44:45] op_sel_hi:[1,0,0]
	v_lshlrev_b32_e32 v2, 8, v18
	v_mul_f32_e32 v3, 0x4b800000, v0
	v_cmp_gt_f32_e32 vcc, s83, v0
	v_add3_u32 v2, s8, v2, v59
	s_nop 0
	v_cndmask_b32_e32 v0, v0, v3, vcc
	v_rsq_f32_e32 v0, v0
	s_nop 0
	v_mul_f32_e32 v3, 0x45800000, v0
	v_cndmask_b32_e32 v0, v0, v3, vcc
	v_mul_f32_e32 v3, v12, v0
	v_bfe_u32 v4, v3, 16, 1
	v_add3_u32 v3, v3, v4, s84
	ds_write_b16_d16_hi v2, v3
	v_mul_f32_e32 v3, 0x4b800000, v1
	v_cmp_gt_f32_e32 vcc, s83, v1
	v_mul_f32_e32 v0, v28, v0
	s_nop 0
	v_cndmask_b32_e32 v1, v1, v3, vcc
	v_rsq_f32_e32 v1, v1
	v_bfe_u32 v3, v0, 16, 1
	v_add3_u32 v0, v0, v3, s84
	ds_write_b16_d16_hi v2, v0 offset:64
	v_mul_f32_e32 v0, 0x45800000, v1
	v_cndmask_b32_e32 v0, v1, v0, vcc
	v_mul_f32_e32 v1, v13, v0
	v_bfe_u32 v2, v1, 16, 1
	v_add3_u32 v1, v1, v2, s84
	ds_write_b16_d16_hi v58, v1 offset:6400
	v_mul_f32_e32 v2, v29, v0
	v_pk_add_f32 v[0:1], v[34:35], v[6:7]
	s_nop 0
	v_pk_fma_f32 v[0:1], v[0:1], s[44:45], v[44:45] op_sel_hi:[1,0,0]
	s_nop 0
	v_mul_f32_e32 v3, 0x4b800000, v0
	v_cmp_gt_f32_e32 vcc, s83, v0
	s_nop 1
	v_cndmask_b32_e32 v0, v0, v3, vcc
	v_rsq_f32_e32 v0, v0
	v_bfe_u32 v3, v2, 16, 1
	v_add3_u32 v2, v2, v3, s84
	ds_write_b16_d16_hi v58, v2 offset:6464
	v_mul_f32_e32 v2, 0x45800000, v0
	v_cndmask_b32_e32 v0, v0, v2, vcc
	v_mul_f32_e32 v2, v14, v0
	v_bfe_u32 v3, v2, 16, 1
	v_add3_u32 v2, v2, v3, s84
	ds_write_b16_d16_hi v58, v2 offset:6656
	v_mul_f32_e32 v2, 0x4b800000, v1
	v_cmp_gt_f32_e32 vcc, s83, v1
	v_mul_f32_e32 v0, v30, v0
	s_nop 0
	v_cndmask_b32_e32 v1, v1, v2, vcc
	v_rsq_f32_e32 v1, v1
	v_bfe_u32 v2, v0, 16, 1
	v_add3_u32 v0, v0, v2, s84
	ds_write_b16_d16_hi v58, v0 offset:6720
	v_mul_f32_e32 v0, 0x45800000, v1
	v_cndmask_b32_e32 v0, v1, v0, vcc
	v_mul_f32_e32 v1, v15, v0
	v_bfe_u32 v2, v1, 16, 1
	v_add3_u32 v1, v1, v2, s84
	v_mul_f32_e32 v0, v31, v0
	ds_write_b16_d16_hi v58, v1 offset:6912
	v_bfe_u32 v1, v0, 16, 1
	v_add3_u32 v0, v0, v1, s84
	v_cmp_gt_i32_e32 vcc, s85, v158
	ds_write_b16_d16_hi v58, v0 offset:6976
	s_waitcnt lgkmcnt(0)
	s_barrier
	s_and_saveexec_b64 s[48:49], vcc
	s_cbranch_execz .LBB0_3192
	s_lshl_b64 s[6:7], s[40:41], 2
	s_add_u32 s4, s4, s6
	s_addc_u32 s5, s5, s7
	s_add_u32 s6, s65, s89
	s_addc_u32 s7, s66, 0
	s_add_u32 s6, s6, s40
	v_and_b32_e32 v2, 15, v158
	s_addc_u32 s7, s7, 0
	v_lshlrev_b32_e32 v0, 4, v2
	v_lshlrev_b32_e32 v156, 3, v2
	v_mov_b32_e32 v1, v157
	v_lshlrev_b32_e32 v2, 5, v2
	v_mov_b32_e32 v3, v157
	v_add_u32_e32 v8, 0, v0
	v_lshl_add_u64 v[0:1], v[160:161], 0, v[0:1]
	v_lshl_add_u64 v[2:3], s[4:5], 0, v[2:3]
	v_lshl_add_u64 v[4:5], s[6:7], 0, v[156:157]
	s_mov_b64 s[50:51], 0
	s_mov_b32 s98, 0xbfb8aa3b
	s_mov_b32 s100, 0x41800000
	v_ashrrev_i32_e32 v6, 4, v158
	global_load_dwordx4 v[36:39], v[2:3], off offset:2064
	global_load_dwordx4 v[32:35], v[2:3], off offset:2048
	v_mad_i64_i32 v[18:19], s[4:5], v6, s71, v[0:1]
	global_load_dwordx4 v[40:43], v[18:19], off offset:3072
	v_add_u32_e32 v9, 32, v6
	v_mad_i64_i32 v[20:21], s[4:5], v9, s71, v[0:1]
	global_load_dwordx4 v[44:47], v[20:21], off offset:3072
	v_add_u32_e32 v9, 64, v6
	v_mad_i64_i32 v[18:19], s[4:5], v9, s71, v[0:1]
	global_load_dwordx4 v[48:51], v[18:19], off offset:3072
	v_add_u32_e32 v9, 96, v6
	v_mad_i64_i32 v[20:21], s[4:5], v9, s71, v[0:1]
	global_load_dwordx4 v[52:55], v[20:21], off offset:3072
	v_lshl_add_u32 v7, v6, 8, v8
	ds_read_b128 v[22:25], v7
	s_waitcnt vmcnt(3) lgkmcnt(0)
; #define LAS __attribute__((address_space(3)))
; __device__ __forceinline__ float sigmoidf_(float x) { return 1.f / (1.f + __expf(-x)); }
; __device__ __forceinline__ unsigned pk4_fp8c(float a, float b, float c, float d) { return pk4_fp8(__builtin_amdgcn_fmed3f(a, -448.f, 448.f), __builtin_amdgcn_fmed3f(b, -448.f, 448.f), __builtin_amdgcn_fmed3f(c, -448.f, 448.f), __builtin_amdgcn_fmed3f(d, -448.f, 448.f)); }
; __device__ __forceinline__ void out_unit_m(LAS unsigned char* lds, LAS unsigned char* ldstab, const OutArgs a, const int wv) {
;     ...
; #pragma unroll 1
;     for (int id = tid; id < 128 * 16; id += 512) { const int row = id >> 4, ch = id & 15;
;         const u32x4 y = *(const LAS u32x4*)(lds + row * TP + ch * 16); const u32x4 g = *(const u32x4*)(a.G + (size_t)row * a.ldg + 8 * ch);
;         const f32x4 g0 = *(const f32x4*)(a.gain + 8 * ch), g1 = *(const f32x4*)(a.gain + 8 * ch + 4);
;         const float yv[8] = {bf_lo(y.x), bf_hi(y.x), bf_lo(y.y), bf_hi(y.y), bf_lo(y.z), bf_hi(y.z), bf_lo(y.w), bf_hi(y.w)};
;         const float gv[8] = {bf_lo(g.x), bf_hi(g.x), bf_lo(g.y), bf_hi(g.y), bf_lo(g.z), bf_hi(g.z), bf_lo(g.w), bf_hi(g.w)};
;         const float gn[8] = {g0[0], g0[1], g0[2], g0[3], g1[0], g1[1], g1[2], g1[3]};
;         float ov[8];
; #pragma unroll
;         for (int i = 0; i < 8; ++i) ov[i] = yv[i] * gn[i] * sigmoidf_(gv[i]);
;         u32x2 w; w.x = pg8::pk4_fp8c(ov[0] * a.oscale, ov[1] * a.oscale, ov[2] * a.oscale, ov[3] * a.oscale); w.y = pg8::pk4_fp8c(ov[4] * a.oscale, ov[5] * a.oscale, ov[6] * a.oscale, ov[7] * a.oscale);
;         *(u32x2*)(a.Out + (size_t)row * a.ldo + 8 * ch) = w; }
	v_lshlrev_b32_e32 v10, 16, v22
	v_and_b32_e32 v11, 0xffff0000, v22
	v_lshlrev_b32_e32 v12, 16, v23
	v_and_b32_e32 v13, 0xffff0000, v23
	v_lshlrev_b32_e32 v14, 16, v24
	v_and_b32_e32 v15, 0xffff0000, v24
	v_lshlrev_b32_e32 v16, 16, v25
	v_and_b32_e32 v17, 0xffff0000, v25
	v_pk_mul_f32 v[10:11], v[32:33], v[10:11]
	v_pk_mul_f32 v[12:13], v[34:35], v[12:13]
	v_pk_mul_f32 v[14:15], v[36:37], v[14:15]
	v_pk_mul_f32 v[16:17], v[38:39], v[16:17]
	v_lshlrev_b32_e32 v56, 16, v40
	v_and_b32_e32 v57, 0xffff0000, v40
	v_lshlrev_b32_e32 v58, 16, v41
	v_and_b32_e32 v59, 0xffff0000, v41
	v_pk_mul_f32 v[56:57], v[56:57], s[98:99] op_sel_hi:[1,0]
	v_pk_mul_f32 v[58:59], v[58:59], s[98:99] op_sel_hi:[1,0]
	v_exp_f32_e32 v56, v56
	v_exp_f32_e32 v57, v57
	v_exp_f32_e32 v58, v58
	v_exp_f32_e32 v59, v59
	v_pk_add_f32 v[56:57], v[56:57], 1.0 op_sel_hi:[1,0]
	v_pk_add_f32 v[58:59], v[58:59], 1.0 op_sel_hi:[1,0]
	v_rcp_f32_e32 v60, v56
	v_rcp_f32_e32 v61, v57
	v_rcp_f32_e32 v62, v58
	v_rcp_f32_e32 v63, v59
	v_pk_fma_f32 v[28:29], v[56:57], v[60:61], 1.0 op_sel_hi:[1,1,0] neg_lo:[1,0,0] neg_hi:[1,0,0]
	v_pk_fma_f32 v[30:31], v[58:59], v[62:63], 1.0 op_sel_hi:[1,1,0] neg_lo:[1,0,0] neg_hi:[1,0,0]
	s_nop 0
	v_pk_fma_f32 v[60:61], v[28:29], v[60:61], v[60:61]
	v_pk_fma_f32 v[62:63], v[30:31], v[62:63], v[62:63]
	s_nop 0
	v_pk_fma_f32 v[28:29], v[56:57], v[60:61], 1.0 op_sel_hi:[1,1,0] neg_lo:[1,0,0] neg_hi:[1,0,0]
	v_pk_fma_f32 v[30:31], v[58:59], v[62:63], 1.0 op_sel_hi:[1,1,0] neg_lo:[1,0,0] neg_hi:[1,0,0]
	s_nop 0
	v_pk_fma_f32 v[64:65], v[28:29], v[60:61], v[60:61]
	v_pk_fma_f32 v[66:67], v[30:31], v[62:63], v[62:63]
	s_nop 0
	v_pk_fma_f32 v[28:29], v[56:57], v[64:65], 1.0 op_sel_hi:[1,1,0] neg_lo:[1,0,0] neg_hi:[1,0,0]
	v_pk_fma_f32 v[30:31], v[58:59], v[66:67], 1.0 op_sel_hi:[1,1,0] neg_lo:[1,0,0] neg_hi:[1,0,0]
	s_nop 0
	v_pk_fma_f32 v[28:29], v[28:29], v[60:61], v[64:65]
	v_pk_fma_f32 v[30:31], v[30:31], v[62:63], v[66:67]
	v_div_fixup_f32 v28, v28, v56, 1.0
	v_div_fixup_f32 v29, v29, v57, 1.0
	v_div_fixup_f32 v30, v30, v58, 1.0
	v_div_fixup_f32 v31, v31, v59, 1.0
	v_pk_mul_f32 v[10:11], v[10:11], v[28:29]
	v_pk_mul_f32 v[12:13], v[12:13], v[30:31]
	v_lshlrev_b32_e32 v56, 16, v42
	v_and_b32_e32 v57, 0xffff0000, v42
	v_lshlrev_b32_e32 v58, 16, v43
	v_and_b32_e32 v59, 0xffff0000, v43
	v_pk_mul_f32 v[56:57], v[56:57], s[98:99] op_sel_hi:[1,0]
	v_pk_mul_f32 v[58:59], v[58:59], s[98:99] op_sel_hi:[1,0]
	v_exp_f32_e32 v56, v56
	v_exp_f32_e32 v57, v57
	v_exp_f32_e32 v58, v58
	v_exp_f32_e32 v59, v59
	v_pk_add_f32 v[56:57], v[56:57], 1.0 op_sel_hi:[1,0]
	v_pk_add_f32 v[58:59], v[58:59], 1.0 op_sel_hi:[1,0]
	v_rcp_f32_e32 v60, v56
	v_rcp_f32_e32 v61, v57
	v_rcp_f32_e32 v62, v58
	v_rcp_f32_e32 v63, v59
	v_pk_fma_f32 v[28:29], v[56:57], v[60:61], 1.0 op_sel_hi:[1,1,0] neg_lo:[1,0,0] neg_hi:[1,0,0]
	v_pk_fma_f32 v[30:31], v[58:59], v[62:63], 1.0 op_sel_hi:[1,1,0] neg_lo:[1,0,0] neg_hi:[1,0,0]
	s_nop 0
	v_pk_fma_f32 v[60:61], v[28:29], v[60:61], v[60:61]
	v_pk_fma_f32 v[62:63], v[30:31], v[62:63], v[62:63]
	s_nop 0
	v_pk_fma_f32 v[28:29], v[56:57], v[60:61], 1.0 op_sel_hi:[1,1,0] neg_lo:[1,0,0] neg_hi:[1,0,0]
	v_pk_fma_f32 v[30:31], v[58:59], v[62:63], 1.0 op_sel_hi:[1,1,0] neg_lo:[1,0,0] neg_hi:[1,0,0]
	s_nop 0
	v_pk_fma_f32 v[64:65], v[28:29], v[60:61], v[60:61]
	v_pk_fma_f32 v[66:67], v[30:31], v[62:63], v[62:63]
	s_nop 0
	v_pk_fma_f32 v[28:29], v[56:57], v[64:65], 1.0 op_sel_hi:[1,1,0] neg_lo:[1,0,0] neg_hi:[1,0,0]
	v_pk_fma_f32 v[30:31], v[58:59], v[66:67], 1.0 op_sel_hi:[1,1,0] neg_lo:[1,0,0] neg_hi:[1,0,0]
	s_nop 0
	v_pk_fma_f32 v[28:29], v[28:29], v[60:61], v[64:65]
	v_pk_fma_f32 v[30:31], v[30:31], v[62:63], v[66:67]
	v_div_fixup_f32 v28, v28, v56, 1.0
	v_div_fixup_f32 v29, v29, v57, 1.0
	v_div_fixup_f32 v30, v30, v58, 1.0
	v_div_fixup_f32 v31, v31, v59, 1.0
	v_pk_mul_f32 v[14:15], v[14:15], v[28:29]
	v_pk_mul_f32 v[16:17], v[16:17], v[30:31]
	v_pk_mul_f32 v[10:11], v[10:11], s[100:101] op_sel_hi:[1,0]
	v_pk_mul_f32 v[12:13], v[12:13], s[100:101] op_sel_hi:[1,0]
	v_pk_mul_f32 v[14:15], v[14:15], s[100:101] op_sel_hi:[1,0]
	v_pk_mul_f32 v[16:17], v[16:17], s[100:101] op_sel_hi:[1,0]
	v_med3_f32 v10, v10, s86, v202
	v_med3_f32 v11, v11, s86, v202
	v_med3_f32 v12, v12, s86, v202
	v_med3_f32 v13, v13, s86, v202
	v_med3_f32 v14, v14, s86, v202
	v_med3_f32 v15, v15, s86, v202
	v_med3_f32 v16, v16, s86, v202
	v_med3_f32 v17, v17, s86, v202
	v_mov_b32_e32 v20, v6
	v_mov_b32_e32 v21, 0
	v_cvt_pk_fp8_f32 v26, v10, v11
	v_cvt_pk_fp8_f32 v27, v14, v15
	v_lshlrev_b64 v[20:21], 10, v[20:21]
	v_cvt_pk_fp8_f32 v26, v12, v13 op_sel:[0,0,1]
	v_cvt_pk_fp8_f32 v27, v16, v17 op_sel:[0,0,1]
	v_lshl_add_u64 v[20:21], v[4:5], 0, v[20:21]
	s_nop 0
	global_store_dwordx2 v[20:21], v[26:27], off
	v_add_u32_e32 v9, 32, v6
	v_lshl_add_u32 v7, v9, 8, v8
	ds_read_b128 v[22:25], v7
	s_waitcnt vmcnt(3) lgkmcnt(0)
; #define LAS __attribute__((address_space(3)))
; __device__ __forceinline__ float sigmoidf_(float x) { return 1.f / (1.f + __expf(-x)); }
; __device__ __forceinline__ unsigned pk4_fp8c(float a, float b, float c, float d) { return pk4_fp8(__builtin_amdgcn_fmed3f(a, -448.f, 448.f), __builtin_amdgcn_fmed3f(b, -448.f, 448.f), __builtin_amdgcn_fmed3f(c, -448.f, 448.f), __builtin_amdgcn_fmed3f(d, -448.f, 448.f)); }
; __device__ __forceinline__ void out_unit_m(LAS unsigned char* lds, LAS unsigned char* ldstab, const OutArgs a, const int wv) {
;     ...
; #pragma unroll 1
;     for (int id = tid; id < 128 * 16; id += 512) { const int row = id >> 4, ch = id & 15;
;         const u32x4 y = *(const LAS u32x4*)(lds + row * TP + ch * 16); const u32x4 g = *(const u32x4*)(a.G + (size_t)row * a.ldg + 8 * ch);
;         const f32x4 g0 = *(const f32x4*)(a.gain + 8 * ch), g1 = *(const f32x4*)(a.gain + 8 * ch + 4);
;         const float yv[8] = {bf_lo(y.x), bf_hi(y.x), bf_lo(y.y), bf_hi(y.y), bf_lo(y.z), bf_hi(y.z), bf_lo(y.w), bf_hi(y.w)};
;         const float gv[8] = {bf_lo(g.x), bf_hi(g.x), bf_lo(g.y), bf_hi(g.y), bf_lo(g.z), bf_hi(g.z), bf_lo(g.w), bf_hi(g.w)};
;         const float gn[8] = {g0[0], g0[1], g0[2], g0[3], g1[0], g1[1], g1[2], g1[3]};
;         float ov[8];
; #pragma unroll
;         for (int i = 0; i < 8; ++i) ov[i] = yv[i] * gn[i] * sigmoidf_(gv[i]);
;         u32x2 w; w.x = pg8::pk4_fp8c(ov[0] * a.oscale, ov[1] * a.oscale, ov[2] * a.oscale, ov[3] * a.oscale); w.y = pg8::pk4_fp8c(ov[4] * a.oscale, ov[5] * a.oscale, ov[6] * a.oscale, ov[7] * a.oscale);
;         *(u32x2*)(a.Out + (size_t)row * a.ldo + 8 * ch) = w; }
	v_lshlrev_b32_e32 v10, 16, v22
	v_and_b32_e32 v11, 0xffff0000, v22
	v_lshlrev_b32_e32 v12, 16, v23
	v_and_b32_e32 v13, 0xffff0000, v23
	v_lshlrev_b32_e32 v14, 16, v24
	v_and_b32_e32 v15, 0xffff0000, v24
	v_lshlrev_b32_e32 v16, 16, v25
	v_and_b32_e32 v17, 0xffff0000, v25
	v_pk_mul_f32 v[10:11], v[32:33], v[10:11]
	v_pk_mul_f32 v[12:13], v[34:35], v[12:13]
	v_pk_mul_f32 v[14:15], v[36:37], v[14:15]
	v_pk_mul_f32 v[16:17], v[38:39], v[16:17]
	v_lshlrev_b32_e32 v56, 16, v44
	v_and_b32_e32 v57, 0xffff0000, v44
	v_lshlrev_b32_e32 v58, 16, v45
	v_and_b32_e32 v59, 0xffff0000, v45
	v_pk_mul_f32 v[56:57], v[56:57], s[98:99] op_sel_hi:[1,0]
	v_pk_mul_f32 v[58:59], v[58:59], s[98:99] op_sel_hi:[1,0]
	v_exp_f32_e32 v56, v56
	v_exp_f32_e32 v57, v57
	v_exp_f32_e32 v58, v58
	v_exp_f32_e32 v59, v59
	v_pk_add_f32 v[56:57], v[56:57], 1.0 op_sel_hi:[1,0]
	v_pk_add_f32 v[58:59], v[58:59], 1.0 op_sel_hi:[1,0]
	v_rcp_f32_e32 v60, v56
	v_rcp_f32_e32 v61, v57
	v_rcp_f32_e32 v62, v58
	v_rcp_f32_e32 v63, v59
	v_pk_fma_f32 v[28:29], v[56:57], v[60:61], 1.0 op_sel_hi:[1,1,0] neg_lo:[1,0,0] neg_hi:[1,0,0]
	v_pk_fma_f32 v[30:31], v[58:59], v[62:63], 1.0 op_sel_hi:[1,1,0] neg_lo:[1,0,0] neg_hi:[1,0,0]
	s_nop 0
	v_pk_fma_f32 v[60:61], v[28:29], v[60:61], v[60:61]
	v_pk_fma_f32 v[62:63], v[30:31], v[62:63], v[62:63]
	s_nop 0
	v_pk_fma_f32 v[28:29], v[56:57], v[60:61], 1.0 op_sel_hi:[1,1,0] neg_lo:[1,0,0] neg_hi:[1,0,0]
	v_pk_fma_f32 v[30:31], v[58:59], v[62:63], 1.0 op_sel_hi:[1,1,0] neg_lo:[1,0,0] neg_hi:[1,0,0]
	s_nop 0
	v_pk_fma_f32 v[64:65], v[28:29], v[60:61], v[60:61]
	v_pk_fma_f32 v[66:67], v[30:31], v[62:63], v[62:63]
	s_nop 0
	v_pk_fma_f32 v[28:29], v[56:57], v[64:65], 1.0 op_sel_hi:[1,1,0] neg_lo:[1,0,0] neg_hi:[1,0,0]
	v_pk_fma_f32 v[30:31], v[58:59], v[66:67], 1.0 op_sel_hi:[1,1,0] neg_lo:[1,0,0] neg_hi:[1,0,0]
	s_nop 0
	v_pk_fma_f32 v[28:29], v[28:29], v[60:61], v[64:65]
	v_pk_fma_f32 v[30:31], v[30:31], v[62:63], v[66:67]
	v_div_fixup_f32 v28, v28, v56, 1.0
	v_div_fixup_f32 v29, v29, v57, 1.0
	v_div_fixup_f32 v30, v30, v58, 1.0
	v_div_fixup_f32 v31, v31, v59, 1.0
	v_pk_mul_f32 v[10:11], v[10:11], v[28:29]
	v_pk_mul_f32 v[12:13], v[12:13], v[30:31]
	v_lshlrev_b32_e32 v56, 16, v46
	v_and_b32_e32 v57, 0xffff0000, v46
	v_lshlrev_b32_e32 v58, 16, v47
	v_and_b32_e32 v59, 0xffff0000, v47
	v_pk_mul_f32 v[56:57], v[56:57], s[98:99] op_sel_hi:[1,0]
	v_pk_mul_f32 v[58:59], v[58:59], s[98:99] op_sel_hi:[1,0]
	v_exp_f32_e32 v56, v56
	v_exp_f32_e32 v57, v57
	v_exp_f32_e32 v58, v58
	v_exp_f32_e32 v59, v59
	v_pk_add_f32 v[56:57], v[56:57], 1.0 op_sel_hi:[1,0]
	v_pk_add_f32 v[58:59], v[58:59], 1.0 op_sel_hi:[1,0]
	v_rcp_f32_e32 v60, v56
	v_rcp_f32_e32 v61, v57
	v_rcp_f32_e32 v62, v58
	v_rcp_f32_e32 v63, v59
	v_pk_fma_f32 v[28:29], v[56:57], v[60:61], 1.0 op_sel_hi:[1,1,0] neg_lo:[1,0,0] neg_hi:[1,0,0]
	v_pk_fma_f32 v[30:31], v[58:59], v[62:63], 1.0 op_sel_hi:[1,1,0] neg_lo:[1,0,0] neg_hi:[1,0,0]
	s_nop 0
	v_pk_fma_f32 v[60:61], v[28:29], v[60:61], v[60:61]
	v_pk_fma_f32 v[62:63], v[30:31], v[62:63], v[62:63]
	s_nop 0
	v_pk_fma_f32 v[28:29], v[56:57], v[60:61], 1.0 op_sel_hi:[1,1,0] neg_lo:[1,0,0] neg_hi:[1,0,0]
	v_pk_fma_f32 v[30:31], v[58:59], v[62:63], 1.0 op_sel_hi:[1,1,0] neg_lo:[1,0,0] neg_hi:[1,0,0]
	s_nop 0
	v_pk_fma_f32 v[64:65], v[28:29], v[60:61], v[60:61]
	v_pk_fma_f32 v[66:67], v[30:31], v[62:63], v[62:63]
	s_nop 0
	v_pk_fma_f32 v[28:29], v[56:57], v[64:65], 1.0 op_sel_hi:[1,1,0] neg_lo:[1,0,0] neg_hi:[1,0,0]
	v_pk_fma_f32 v[30:31], v[58:59], v[66:67], 1.0 op_sel_hi:[1,1,0] neg_lo:[1,0,0] neg_hi:[1,0,0]
	s_nop 0
	v_pk_fma_f32 v[28:29], v[28:29], v[60:61], v[64:65]
	v_pk_fma_f32 v[30:31], v[30:31], v[62:63], v[66:67]
	v_div_fixup_f32 v28, v28, v56, 1.0
	v_div_fixup_f32 v29, v29, v57, 1.0
	v_div_fixup_f32 v30, v30, v58, 1.0
	v_div_fixup_f32 v31, v31, v59, 1.0
	v_pk_mul_f32 v[14:15], v[14:15], v[28:29]
	v_pk_mul_f32 v[16:17], v[16:17], v[30:31]
	v_pk_mul_f32 v[10:11], v[10:11], s[100:101] op_sel_hi:[1,0]
	v_pk_mul_f32 v[12:13], v[12:13], s[100:101] op_sel_hi:[1,0]
	v_pk_mul_f32 v[14:15], v[14:15], s[100:101] op_sel_hi:[1,0]
	v_pk_mul_f32 v[16:17], v[16:17], s[100:101] op_sel_hi:[1,0]
	v_med3_f32 v10, v10, s86, v202
	v_med3_f32 v11, v11, s86, v202
	v_med3_f32 v12, v12, s86, v202
	v_med3_f32 v13, v13, s86, v202
	v_med3_f32 v14, v14, s86, v202
	v_med3_f32 v15, v15, s86, v202
	v_med3_f32 v16, v16, s86, v202
	v_med3_f32 v17, v17, s86, v202
	v_add_u32_e32 v20, 32, v6
	v_mov_b32_e32 v21, 0
	v_cvt_pk_fp8_f32 v26, v10, v11
	v_cvt_pk_fp8_f32 v27, v14, v15
	v_lshlrev_b64 v[20:21], 10, v[20:21]
	v_cvt_pk_fp8_f32 v26, v12, v13 op_sel:[0,0,1]
	v_cvt_pk_fp8_f32 v27, v16, v17 op_sel:[0,0,1]
	v_lshl_add_u64 v[20:21], v[4:5], 0, v[20:21]
	s_nop 0
	global_store_dwordx2 v[20:21], v[26:27], off
	v_add_u32_e32 v9, 64, v6
	v_lshl_add_u32 v7, v9, 8, v8
	ds_read_b128 v[22:25], v7
	s_waitcnt vmcnt(3) lgkmcnt(0)
; #define LAS __attribute__((address_space(3)))
; __device__ __forceinline__ float sigmoidf_(float x) { return 1.f / (1.f + __expf(-x)); }
; __device__ __forceinline__ unsigned pk4_fp8c(float a, float b, float c, float d) { return pk4_fp8(__builtin_amdgcn_fmed3f(a, -448.f, 448.f), __builtin_amdgcn_fmed3f(b, -448.f, 448.f), __builtin_amdgcn_fmed3f(c, -448.f, 448.f), __builtin_amdgcn_fmed3f(d, -448.f, 448.f)); }
; __device__ __forceinline__ void out_unit_m(LAS unsigned char* lds, LAS unsigned char* ldstab, const OutArgs a, const int wv) {
;     ...
; #pragma unroll 1
;     for (int id = tid; id < 128 * 16; id += 512) { const int row = id >> 4, ch = id & 15;
;         const u32x4 y = *(const LAS u32x4*)(lds + row * TP + ch * 16); const u32x4 g = *(const u32x4*)(a.G + (size_t)row * a.ldg + 8 * ch);
;         const f32x4 g0 = *(const f32x4*)(a.gain + 8 * ch), g1 = *(const f32x4*)(a.gain + 8 * ch + 4);
;         const float yv[8] = {bf_lo(y.x), bf_hi(y.x), bf_lo(y.y), bf_hi(y.y), bf_lo(y.z), bf_hi(y.z), bf_lo(y.w), bf_hi(y.w)};
;         const float gv[8] = {bf_lo(g.x), bf_hi(g.x), bf_lo(g.y), bf_hi(g.y), bf_lo(g.z), bf_hi(g.z), bf_lo(g.w), bf_hi(g.w)};
;         const float gn[8] = {g0[0], g0[1], g0[2], g0[3], g1[0], g1[1], g1[2], g1[3]};
;         float ov[8];
; #pragma unroll
;         for (int i = 0; i < 8; ++i) ov[i] = yv[i] * gn[i] * sigmoidf_(gv[i]);
;         u32x2 w; w.x = pg8::pk4_fp8c(ov[0] * a.oscale, ov[1] * a.oscale, ov[2] * a.oscale, ov[3] * a.oscale); w.y = pg8::pk4_fp8c(ov[4] * a.oscale, ov[5] * a.oscale, ov[6] * a.oscale, ov[7] * a.oscale);
;         *(u32x2*)(a.Out + (size_t)row * a.ldo + 8 * ch) = w; }
	v_lshlrev_b32_e32 v10, 16, v22
	v_and_b32_e32 v11, 0xffff0000, v22
	v_lshlrev_b32_e32 v12, 16, v23
	v_and_b32_e32 v13, 0xffff0000, v23
	v_lshlrev_b32_e32 v14, 16, v24
	v_and_b32_e32 v15, 0xffff0000, v24
	v_lshlrev_b32_e32 v16, 16, v25
	v_and_b32_e32 v17, 0xffff0000, v25
	v_pk_mul_f32 v[10:11], v[32:33], v[10:11]
	v_pk_mul_f32 v[12:13], v[34:35], v[12:13]
	v_pk_mul_f32 v[14:15], v[36:37], v[14:15]
	v_pk_mul_f32 v[16:17], v[38:39], v[16:17]
	v_lshlrev_b32_e32 v56, 16, v48
	v_and_b32_e32 v57, 0xffff0000, v48
	v_lshlrev_b32_e32 v58, 16, v49
	v_and_b32_e32 v59, 0xffff0000, v49
	v_pk_mul_f32 v[56:57], v[56:57], s[98:99] op_sel_hi:[1,0]
	v_pk_mul_f32 v[58:59], v[58:59], s[98:99] op_sel_hi:[1,0]
	v_exp_f32_e32 v56, v56
	v_exp_f32_e32 v57, v57
	v_exp_f32_e32 v58, v58
	v_exp_f32_e32 v59, v59
	v_pk_add_f32 v[56:57], v[56:57], 1.0 op_sel_hi:[1,0]
	v_pk_add_f32 v[58:59], v[58:59], 1.0 op_sel_hi:[1,0]
	v_rcp_f32_e32 v60, v56
	v_rcp_f32_e32 v61, v57
	v_rcp_f32_e32 v62, v58
	v_rcp_f32_e32 v63, v59
	v_pk_fma_f32 v[28:29], v[56:57], v[60:61], 1.0 op_sel_hi:[1,1,0] neg_lo:[1,0,0] neg_hi:[1,0,0]
	v_pk_fma_f32 v[30:31], v[58:59], v[62:63], 1.0 op_sel_hi:[1,1,0] neg_lo:[1,0,0] neg_hi:[1,0,0]
	s_nop 0
	v_pk_fma_f32 v[60:61], v[28:29], v[60:61], v[60:61]
	v_pk_fma_f32 v[62:63], v[30:31], v[62:63], v[62:63]
	s_nop 0
	v_pk_fma_f32 v[28:29], v[56:57], v[60:61], 1.0 op_sel_hi:[1,1,0] neg_lo:[1,0,0] neg_hi:[1,0,0]
	v_pk_fma_f32 v[30:31], v[58:59], v[62:63], 1.0 op_sel_hi:[1,1,0] neg_lo:[1,0,0] neg_hi:[1,0,0]
	s_nop 0
	v_pk_fma_f32 v[64:65], v[28:29], v[60:61], v[60:61]
	v_pk_fma_f32 v[66:67], v[30:31], v[62:63], v[62:63]
	s_nop 0
	v_pk_fma_f32 v[28:29], v[56:57], v[64:65], 1.0 op_sel_hi:[1,1,0] neg_lo:[1,0,0] neg_hi:[1,0,0]
	v_pk_fma_f32 v[30:31], v[58:59], v[66:67], 1.0 op_sel_hi:[1,1,0] neg_lo:[1,0,0] neg_hi:[1,0,0]
	s_nop 0
	v_pk_fma_f32 v[28:29], v[28:29], v[60:61], v[64:65]
	v_pk_fma_f32 v[30:31], v[30:31], v[62:63], v[66:67]
	v_div_fixup_f32 v28, v28, v56, 1.0
	v_div_fixup_f32 v29, v29, v57, 1.0
	v_div_fixup_f32 v30, v30, v58, 1.0
	v_div_fixup_f32 v31, v31, v59, 1.0
	v_pk_mul_f32 v[10:11], v[10:11], v[28:29]
	v_pk_mul_f32 v[12:13], v[12:13], v[30:31]
	v_lshlrev_b32_e32 v56, 16, v50
	v_and_b32_e32 v57, 0xffff0000, v50
	v_lshlrev_b32_e32 v58, 16, v51
	v_and_b32_e32 v59, 0xffff0000, v51
	v_pk_mul_f32 v[56:57], v[56:57], s[98:99] op_sel_hi:[1,0]
	v_pk_mul_f32 v[58:59], v[58:59], s[98:99] op_sel_hi:[1,0]
	v_exp_f32_e32 v56, v56
	v_exp_f32_e32 v57, v57
	v_exp_f32_e32 v58, v58
	v_exp_f32_e32 v59, v59
	v_pk_add_f32 v[56:57], v[56:57], 1.0 op_sel_hi:[1,0]
	v_pk_add_f32 v[58:59], v[58:59], 1.0 op_sel_hi:[1,0]
	v_rcp_f32_e32 v60, v56
	v_rcp_f32_e32 v61, v57
	v_rcp_f32_e32 v62, v58
	v_rcp_f32_e32 v63, v59
	v_pk_fma_f32 v[28:29], v[56:57], v[60:61], 1.0 op_sel_hi:[1,1,0] neg_lo:[1,0,0] neg_hi:[1,0,0]
	v_pk_fma_f32 v[30:31], v[58:59], v[62:63], 1.0 op_sel_hi:[1,1,0] neg_lo:[1,0,0] neg_hi:[1,0,0]
	s_nop 0
	v_pk_fma_f32 v[60:61], v[28:29], v[60:61], v[60:61]
	v_pk_fma_f32 v[62:63], v[30:31], v[62:63], v[62:63]
	s_nop 0
	v_pk_fma_f32 v[28:29], v[56:57], v[60:61], 1.0 op_sel_hi:[1,1,0] neg_lo:[1,0,0] neg_hi:[1,0,0]
	v_pk_fma_f32 v[30:31], v[58:59], v[62:63], 1.0 op_sel_hi:[1,1,0] neg_lo:[1,0,0] neg_hi:[1,0,0]
	s_nop 0
	v_pk_fma_f32 v[64:65], v[28:29], v[60:61], v[60:61]
	v_pk_fma_f32 v[66:67], v[30:31], v[62:63], v[62:63]
	s_nop 0
	v_pk_fma_f32 v[28:29], v[56:57], v[64:65], 1.0 op_sel_hi:[1,1,0] neg_lo:[1,0,0] neg_hi:[1,0,0]
	v_pk_fma_f32 v[30:31], v[58:59], v[66:67], 1.0 op_sel_hi:[1,1,0] neg_lo:[1,0,0] neg_hi:[1,0,0]
	s_nop 0
	v_pk_fma_f32 v[28:29], v[28:29], v[60:61], v[64:65]
	v_pk_fma_f32 v[30:31], v[30:31], v[62:63], v[66:67]
	v_div_fixup_f32 v28, v28, v56, 1.0
	v_div_fixup_f32 v29, v29, v57, 1.0
	v_div_fixup_f32 v30, v30, v58, 1.0
	v_div_fixup_f32 v31, v31, v59, 1.0
	v_pk_mul_f32 v[14:15], v[14:15], v[28:29]
	v_pk_mul_f32 v[16:17], v[16:17], v[30:31]
	v_pk_mul_f32 v[10:11], v[10:11], s[100:101] op_sel_hi:[1,0]
	v_pk_mul_f32 v[12:13], v[12:13], s[100:101] op_sel_hi:[1,0]
	v_pk_mul_f32 v[14:15], v[14:15], s[100:101] op_sel_hi:[1,0]
	v_pk_mul_f32 v[16:17], v[16:17], s[100:101] op_sel_hi:[1,0]
	v_med3_f32 v10, v10, s86, v202
	v_med3_f32 v11, v11, s86, v202
	v_med3_f32 v12, v12, s86, v202
	v_med3_f32 v13, v13, s86, v202
	v_med3_f32 v14, v14, s86, v202
	v_med3_f32 v15, v15, s86, v202
	v_med3_f32 v16, v16, s86, v202
	v_med3_f32 v17, v17, s86, v202
	v_add_u32_e32 v20, 64, v6
	v_mov_b32_e32 v21, 0
	v_cvt_pk_fp8_f32 v26, v10, v11
	v_cvt_pk_fp8_f32 v27, v14, v15
	v_lshlrev_b64 v[20:21], 10, v[20:21]
	v_cvt_pk_fp8_f32 v26, v12, v13 op_sel:[0,0,1]
	v_cvt_pk_fp8_f32 v27, v16, v17 op_sel:[0,0,1]
	v_lshl_add_u64 v[20:21], v[4:5], 0, v[20:21]
	s_nop 0
	global_store_dwordx2 v[20:21], v[26:27], off
	v_add_u32_e32 v9, 96, v6
	v_lshl_add_u32 v7, v9, 8, v8
	ds_read_b128 v[22:25], v7
	s_waitcnt vmcnt(3) lgkmcnt(0)
; #define LAS __attribute__((address_space(3)))
; __device__ __forceinline__ float sigmoidf_(float x) { return 1.f / (1.f + __expf(-x)); }
; __device__ __forceinline__ unsigned pk4_fp8c(float a, float b, float c, float d) { return pk4_fp8(__builtin_amdgcn_fmed3f(a, -448.f, 448.f), __builtin_amdgcn_fmed3f(b, -448.f, 448.f), __builtin_amdgcn_fmed3f(c, -448.f, 448.f), __builtin_amdgcn_fmed3f(d, -448.f, 448.f)); }
; __device__ __forceinline__ void out_unit_m(LAS unsigned char* lds, LAS unsigned char* ldstab, const OutArgs a, const int wv) {
;     ...
; #pragma unroll 1
;     for (int id = tid; id < 128 * 16; id += 512) { const int row = id >> 4, ch = id & 15;
;         const u32x4 y = *(const LAS u32x4*)(lds + row * TP + ch * 16); const u32x4 g = *(const u32x4*)(a.G + (size_t)row * a.ldg + 8 * ch);
;         const f32x4 g0 = *(const f32x4*)(a.gain + 8 * ch), g1 = *(const f32x4*)(a.gain + 8 * ch + 4);
;         const float yv[8] = {bf_lo(y.x), bf_hi(y.x), bf_lo(y.y), bf_hi(y.y), bf_lo(y.z), bf_hi(y.z), bf_lo(y.w), bf_hi(y.w)};
;         const float gv[8] = {bf_lo(g.x), bf_hi(g.x), bf_lo(g.y), bf_hi(g.y), bf_lo(g.z), bf_hi(g.z), bf_lo(g.w), bf_hi(g.w)};
;         const float gn[8] = {g0[0], g0[1], g0[2], g0[3], g1[0], g1[1], g1[2], g1[3]};
;         float ov[8];
; #pragma unroll
;         for (int i = 0; i < 8; ++i) ov[i] = yv[i] * gn[i] * sigmoidf_(gv[i]);
;         u32x2 w; w.x = pg8::pk4_fp8c(ov[0] * a.oscale, ov[1] * a.oscale, ov[2] * a.oscale, ov[3] * a.oscale); w.y = pg8::pk4_fp8c(ov[4] * a.oscale, ov[5] * a.oscale, ov[6] * a.oscale, ov[7] * a.oscale);
;         *(u32x2*)(a.Out + (size_t)row * a.ldo + 8 * ch) = w; }
	v_lshlrev_b32_e32 v10, 16, v22
	v_and_b32_e32 v11, 0xffff0000, v22
	v_lshlrev_b32_e32 v12, 16, v23
	v_and_b32_e32 v13, 0xffff0000, v23
	v_lshlrev_b32_e32 v14, 16, v24
	v_and_b32_e32 v15, 0xffff0000, v24
	v_lshlrev_b32_e32 v16, 16, v25
	v_and_b32_e32 v17, 0xffff0000, v25
	v_pk_mul_f32 v[10:11], v[32:33], v[10:11]
	v_pk_mul_f32 v[12:13], v[34:35], v[12:13]
	v_pk_mul_f32 v[14:15], v[36:37], v[14:15]
	v_pk_mul_f32 v[16:17], v[38:39], v[16:17]
	v_lshlrev_b32_e32 v56, 16, v52
	v_and_b32_e32 v57, 0xffff0000, v52
	v_lshlrev_b32_e32 v58, 16, v53
	v_and_b32_e32 v59, 0xffff0000, v53
	v_pk_mul_f32 v[56:57], v[56:57], s[98:99] op_sel_hi:[1,0]
	v_pk_mul_f32 v[58:59], v[58:59], s[98:99] op_sel_hi:[1,0]
	v_exp_f32_e32 v56, v56
	v_exp_f32_e32 v57, v57
	v_exp_f32_e32 v58, v58
	v_exp_f32_e32 v59, v59
	v_pk_add_f32 v[56:57], v[56:57], 1.0 op_sel_hi:[1,0]
	v_pk_add_f32 v[58:59], v[58:59], 1.0 op_sel_hi:[1,0]
	v_rcp_f32_e32 v60, v56
	v_rcp_f32_e32 v61, v57
	v_rcp_f32_e32 v62, v58
	v_rcp_f32_e32 v63, v59
	v_pk_fma_f32 v[28:29], v[56:57], v[60:61], 1.0 op_sel_hi:[1,1,0] neg_lo:[1,0,0] neg_hi:[1,0,0]
	v_pk_fma_f32 v[30:31], v[58:59], v[62:63], 1.0 op_sel_hi:[1,1,0] neg_lo:[1,0,0] neg_hi:[1,0,0]
	s_nop 0
	v_pk_fma_f32 v[60:61], v[28:29], v[60:61], v[60:61]
	v_pk_fma_f32 v[62:63], v[30:31], v[62:63], v[62:63]
	s_nop 0
	v_pk_fma_f32 v[28:29], v[56:57], v[60:61], 1.0 op_sel_hi:[1,1,0] neg_lo:[1,0,0] neg_hi:[1,0,0]
	v_pk_fma_f32 v[30:31], v[58:59], v[62:63], 1.0 op_sel_hi:[1,1,0] neg_lo:[1,0,0] neg_hi:[1,0,0]
	s_nop 0
	v_pk_fma_f32 v[64:65], v[28:29], v[60:61], v[60:61]
	v_pk_fma_f32 v[66:67], v[30:31], v[62:63], v[62:63]
	s_nop 0
	v_pk_fma_f32 v[28:29], v[56:57], v[64:65], 1.0 op_sel_hi:[1,1,0] neg_lo:[1,0,0] neg_hi:[1,0,0]
	v_pk_fma_f32 v[30:31], v[58:59], v[66:67], 1.0 op_sel_hi:[1,1,0] neg_lo:[1,0,0] neg_hi:[1,0,0]
	s_nop 0
	v_pk_fma_f32 v[28:29], v[28:29], v[60:61], v[64:65]
	v_pk_fma_f32 v[30:31], v[30:31], v[62:63], v[66:67]
	v_div_fixup_f32 v28, v28, v56, 1.0
	v_div_fixup_f32 v29, v29, v57, 1.0
	v_div_fixup_f32 v30, v30, v58, 1.0
	v_div_fixup_f32 v31, v31, v59, 1.0
	v_pk_mul_f32 v[10:11], v[10:11], v[28:29]
	v_pk_mul_f32 v[12:13], v[12:13], v[30:31]
	v_lshlrev_b32_e32 v56, 16, v54
	v_and_b32_e32 v57, 0xffff0000, v54
	v_lshlrev_b32_e32 v58, 16, v55
	v_and_b32_e32 v59, 0xffff0000, v55
	v_pk_mul_f32 v[56:57], v[56:57], s[98:99] op_sel_hi:[1,0]
	v_pk_mul_f32 v[58:59], v[58:59], s[98:99] op_sel_hi:[1,0]
	v_exp_f32_e32 v56, v56
	v_exp_f32_e32 v57, v57
	v_exp_f32_e32 v58, v58
	v_exp_f32_e32 v59, v59
	v_pk_add_f32 v[56:57], v[56:57], 1.0 op_sel_hi:[1,0]
	v_pk_add_f32 v[58:59], v[58:59], 1.0 op_sel_hi:[1,0]
	v_rcp_f32_e32 v60, v56
	v_rcp_f32_e32 v61, v57
	v_rcp_f32_e32 v62, v58
	v_rcp_f32_e32 v63, v59
	v_pk_fma_f32 v[28:29], v[56:57], v[60:61], 1.0 op_sel_hi:[1,1,0] neg_lo:[1,0,0] neg_hi:[1,0,0]
	v_pk_fma_f32 v[30:31], v[58:59], v[62:63], 1.0 op_sel_hi:[1,1,0] neg_lo:[1,0,0] neg_hi:[1,0,0]
	s_nop 0
	v_pk_fma_f32 v[60:61], v[28:29], v[60:61], v[60:61]
	v_pk_fma_f32 v[62:63], v[30:31], v[62:63], v[62:63]
	s_nop 0
	v_pk_fma_f32 v[28:29], v[56:57], v[60:61], 1.0 op_sel_hi:[1,1,0] neg_lo:[1,0,0] neg_hi:[1,0,0]
	v_pk_fma_f32 v[30:31], v[58:59], v[62:63], 1.0 op_sel_hi:[1,1,0] neg_lo:[1,0,0] neg_hi:[1,0,0]
	s_nop 0
	v_pk_fma_f32 v[64:65], v[28:29], v[60:61], v[60:61]
	v_pk_fma_f32 v[66:67], v[30:31], v[62:63], v[62:63]
	s_nop 0
	v_pk_fma_f32 v[28:29], v[56:57], v[64:65], 1.0 op_sel_hi:[1,1,0] neg_lo:[1,0,0] neg_hi:[1,0,0]
	v_pk_fma_f32 v[30:31], v[58:59], v[66:67], 1.0 op_sel_hi:[1,1,0] neg_lo:[1,0,0] neg_hi:[1,0,0]
	s_nop 0
	v_pk_fma_f32 v[28:29], v[28:29], v[60:61], v[64:65]
	v_pk_fma_f32 v[30:31], v[30:31], v[62:63], v[66:67]
	v_div_fixup_f32 v28, v28, v56, 1.0
	v_div_fixup_f32 v29, v29, v57, 1.0
	v_div_fixup_f32 v30, v30, v58, 1.0
	v_div_fixup_f32 v31, v31, v59, 1.0
	v_pk_mul_f32 v[14:15], v[14:15], v[28:29]
	v_pk_mul_f32 v[16:17], v[16:17], v[30:31]
	v_pk_mul_f32 v[10:11], v[10:11], s[100:101] op_sel_hi:[1,0]
	v_pk_mul_f32 v[12:13], v[12:13], s[100:101] op_sel_hi:[1,0]
	v_pk_mul_f32 v[14:15], v[14:15], s[100:101] op_sel_hi:[1,0]
	v_pk_mul_f32 v[16:17], v[16:17], s[100:101] op_sel_hi:[1,0]
	v_med3_f32 v10, v10, s86, v202
	v_med3_f32 v11, v11, s86, v202
	v_med3_f32 v12, v12, s86, v202
	v_med3_f32 v13, v13, s86, v202
	v_med3_f32 v14, v14, s86, v202
	v_med3_f32 v15, v15, s86, v202
	v_med3_f32 v16, v16, s86, v202
	v_med3_f32 v17, v17, s86, v202
	v_add_u32_e32 v20, 96, v6
	v_mov_b32_e32 v21, 0
	v_cvt_pk_fp8_f32 v26, v10, v11
	v_cvt_pk_fp8_f32 v27, v14, v15
	v_lshlrev_b64 v[20:21], 10, v[20:21]
	v_cvt_pk_fp8_f32 v26, v12, v13 op_sel:[0,0,1]
	v_cvt_pk_fp8_f32 v27, v16, v17 op_sel:[0,0,1]
	v_lshl_add_u64 v[20:21], v[4:5], 0, v[20:21]
	s_nop 0
	global_store_dwordx2 v[20:21], v[26:27], off
